# ctx-row GEMM tails (merge/wout/expert up/down): k-loop global loads requested two k-tiles earlier into dedicated registers, waits recomputed (on top of v25)
# baseline (speedup 1.0000x reference)
.LBB0_1094:
	s_or_b64 exec, exec, s[14:15]
	s_waitcnt vmcnt(0)
	v_ashrrev_i32_e32 v2, 6, v8
	v_lshrrev_b32_e32 v3, 30, v2
	s_mov_b64 s[14:15], 0x1000000
	v_add_u32_e32 v3, v2, v3
	v_lshl_add_u64 v[62:63], v[6:7], 0, s[14:15]
	v_ashrrev_i32_e32 v6, 2, v3
	v_mul_i32_i24_e32 v3, 4, v6
	v_and_b32_e32 v7, 31, v8
	v_sub_u32_e32 v2, v2, v3
	v_lshrrev_b32_e32 v3, 1, v8
	v_lshl_or_b32 v2, v2, 5, v7
	v_and_b32_e32 v8, 16, v3
	v_mul_lo_u32 v2, v2, s21
	v_add3_u32 v65, 0, v2, v8
	global_load_dwordx4 v[112:115], v[62:63], off offset:128
	global_load_dwordx4 v[116:119], v[58:59], off offset:128
	global_load_dwordx4 v[120:123], v[60:61], off offset:128
	global_load_dwordx4 v[124:127], v[62:63], off offset:256
	global_load_dwordx4 v[128:131], v[58:59], off offset:256
	global_load_dwordx4 v[132:135], v[60:61], off offset:256
	global_load_dwordx4 v[136:139], v[62:63], off offset:384
	global_load_dwordx4 v[140:143], v[58:59], off offset:384
	global_load_dwordx4 v[144:147], v[60:61], off offset:384
	s_waitcnt lgkmcnt(0)
	s_barrier
	global_load_dwordx4 v[100:103], v[62:63], off offset:512
	global_load_dwordx4 v[104:107], v[58:59], off offset:512
	global_load_dwordx4 v[108:111], v[60:61], off offset:512
	ds_read_b128 v[2:5], v65 offset:9280
	v_lshl_or_b32 v6, v6, 5, v7
	v_mul_lo_u32 v6, v6, s21
	v_add3_u32 v66, 0, v6, v8
	ds_read_b128 v[6:9], v66 offset:64
	ds_read_b128 v[18:21], v66 offset:96
	ds_read_b128 v[22:25], v65 offset:9312
	s_waitcnt lgkmcnt(2)
	v_mfma_f32_32x32x16_bf16 v[2:17], v[2:5], v[6:9], 0
	s_waitcnt lgkmcnt(0)
	v_mfma_f32_32x32x16_bf16 v[2:17], v[22:25], v[18:21], v[2:17]
	ds_read_b128 v[18:21], v65 offset:9344
	ds_read_b128 v[26:29], v66 offset:128
	ds_read_b128 v[42:45], v66 offset:160
	ds_read_b128 v[46:49], v65 offset:9376
	s_waitcnt lgkmcnt(2)
	v_mfma_f32_32x32x16_bf16 v[2:17], v[18:21], v[26:29], v[2:17]
	s_waitcnt vmcnt(11)
	ds_write_b128 v55, v[112:115] offset:27712
	s_waitcnt lgkmcnt(1)
	v_mfma_f32_32x32x16_bf16 v[2:17], v[46:49], v[42:45], v[2:17]
	s_and_saveexec_b64 s[14:15], vcc
	s_cbranch_execz .LBB0_1096
	s_waitcnt vmcnt(10)
	ds_write_b128 v55, v[116:119] offset:36928
.LBB0_1096:
	s_or_b64 exec, exec, s[14:15]
	s_and_saveexec_b64 s[14:15], s[0:1]
	s_cbranch_execz .LBB0_1098
	s_waitcnt vmcnt(9)
	ds_write_b128 v57, v[120:123] offset:36928
.LBB0_1098:
	s_or_b64 exec, exec, s[14:15]
	s_waitcnt lgkmcnt(0)
	s_barrier
	global_load_dwordx4 v[112:115], v[62:63], off offset:640
	global_load_dwordx4 v[116:119], v[58:59], off offset:640
	global_load_dwordx4 v[120:123], v[60:61], off offset:640
	ds_read_b128 v[30:33], v65 offset:36928
	ds_read_b128 v[34:37], v66 offset:27712
	ds_read_b128 v[38:41], v66 offset:27744
	ds_read_b128 v[42:45], v65 offset:36960
	s_waitcnt lgkmcnt(2)
	v_mfma_f32_32x32x16_bf16 v[2:17], v[30:33], v[34:37], v[2:17]
	s_waitcnt lgkmcnt(0)
	v_mfma_f32_32x32x16_bf16 v[2:17], v[42:45], v[38:41], v[2:17]
	ds_read_b128 v[30:33], v65 offset:36992
	ds_read_b128 v[38:41], v66 offset:27776
	ds_read_b128 v[42:45], v66 offset:27808
	ds_read_b128 v[46:49], v65 offset:37024
	s_waitcnt lgkmcnt(2)
	v_mfma_f32_32x32x16_bf16 v[2:17], v[30:33], v[38:41], v[2:17]
	s_waitcnt vmcnt(11)
	ds_write_b128 v55, v[124:127] offset:64
	s_waitcnt lgkmcnt(1)
	v_mfma_f32_32x32x16_bf16 v[2:17], v[46:49], v[42:45], v[2:17]
	s_and_saveexec_b64 s[14:15], vcc
	s_cbranch_execz .LBB0_1100
	s_waitcnt vmcnt(10)
	ds_write_b128 v55, v[128:131] offset:9280
.LBB0_1100:
	s_or_b64 exec, exec, s[14:15]
	s_and_saveexec_b64 s[14:15], s[0:1]
	s_cbranch_execz .LBB0_1102
	s_waitcnt vmcnt(9)
	ds_write_b128 v57, v[132:135] offset:9280
.LBB0_1102:
	s_or_b64 exec, exec, s[14:15]
	s_waitcnt lgkmcnt(0)
	s_barrier
	global_load_dwordx4 v[124:127], v[62:63], off offset:768
	global_load_dwordx4 v[128:131], v[58:59], off offset:768
	global_load_dwordx4 v[132:135], v[60:61], off offset:768
	ds_read_b128 v[18:21], v65 offset:9280
	ds_read_b128 v[22:25], v66 offset:64
	ds_read_b128 v[26:29], v66 offset:96
	ds_read_b128 v[42:45], v65 offset:9312
	s_waitcnt lgkmcnt(2)
	v_mfma_f32_32x32x16_bf16 v[2:17], v[18:21], v[22:25], v[2:17]
	ds_read_b128 v[18:21], v65 offset:9344
	ds_read_b128 v[22:25], v66 offset:128
	s_waitcnt lgkmcnt(2)
	v_mfma_f32_32x32x16_bf16 v[2:17], v[42:45], v[26:29], v[2:17]
	ds_read_b128 v[42:45], v66 offset:160
	ds_read_b128 v[50:53], v65 offset:9376
	s_waitcnt lgkmcnt(2)
	v_mfma_f32_32x32x16_bf16 v[2:17], v[18:21], v[22:25], v[2:17]
	s_waitcnt vmcnt(11)
	ds_write_b128 v55, v[136:139] offset:27712
	s_waitcnt lgkmcnt(1)
	v_mfma_f32_32x32x16_bf16 v[2:17], v[50:53], v[42:45], v[2:17]
	s_and_saveexec_b64 s[14:15], vcc
	s_cbranch_execz .LBB0_1104
	s_waitcnt vmcnt(10)
	ds_write_b128 v55, v[140:143] offset:36928
.LBB0_1104:
	s_or_b64 exec, exec, s[14:15]
	s_and_saveexec_b64 s[14:15], s[0:1]
	s_cbranch_execz .LBB0_1106
	s_waitcnt vmcnt(9)
	ds_write_b128 v57, v[144:147] offset:36928
.LBB0_1106:
	s_or_b64 exec, exec, s[14:15]
	s_waitcnt lgkmcnt(0)
	s_barrier
	global_load_dwordx4 v[136:139], v[62:63], off offset:896
	global_load_dwordx4 v[140:143], v[58:59], off offset:896
	global_load_dwordx4 v[144:147], v[60:61], off offset:896
	ds_read_b128 v[22:25], v65 offset:36928
	ds_read_b128 v[30:33], v66 offset:27712
	ds_read_b128 v[34:37], v66 offset:27744
	ds_read_b128 v[38:41], v65 offset:36960
	s_waitcnt lgkmcnt(2)
	v_mfma_f32_32x32x16_bf16 v[2:17], v[22:25], v[30:33], v[2:17]
	ds_read_b128 v[22:25], v65 offset:36992
	ds_read_b128 v[30:33], v66 offset:27776
	s_waitcnt lgkmcnt(2)
	v_mfma_f32_32x32x16_bf16 v[2:17], v[38:41], v[34:37], v[2:17]
	ds_read_b128 v[34:37], v66 offset:27808
	ds_read_b128 v[38:41], v65 offset:37024
	s_waitcnt lgkmcnt(2)
	v_mfma_f32_32x32x16_bf16 v[2:17], v[22:25], v[30:33], v[2:17]
	s_waitcnt vmcnt(11)
	ds_write_b128 v55, v[100:103] offset:64
	s_waitcnt lgkmcnt(1)
	v_mfma_f32_32x32x16_bf16 v[2:17], v[38:41], v[34:37], v[2:17]
	s_and_saveexec_b64 s[14:15], vcc
	s_cbranch_execz .LBB0_1108
	s_waitcnt vmcnt(10)
	ds_write_b128 v55, v[104:107] offset:9280
.LBB0_1108:
	s_or_b64 exec, exec, s[14:15]
	s_and_saveexec_b64 s[14:15], s[0:1]
	s_cbranch_execz .LBB0_1110
	s_waitcnt vmcnt(9)
	ds_write_b128 v57, v[108:111] offset:9280
.LBB0_1110:
	s_or_b64 exec, exec, s[14:15]
	s_waitcnt lgkmcnt(0)
	s_barrier
	ds_read_b128 v[18:21], v65 offset:9280
	ds_read_b128 v[26:29], v66 offset:64
	ds_read_b128 v[30:33], v66 offset:96
	ds_read_b128 v[34:37], v65 offset:9312
	s_waitcnt lgkmcnt(2)
	v_mfma_f32_32x32x16_bf16 v[2:17], v[18:21], v[26:29], v[2:17]
	ds_read_b128 v[18:21], v65 offset:9344
	ds_read_b128 v[26:29], v66 offset:128
	s_waitcnt lgkmcnt(2)
	v_mfma_f32_32x32x16_bf16 v[2:17], v[34:37], v[30:33], v[2:17]
	ds_read_b128 v[46:49], v66 offset:160
	ds_read_b128 v[68:71], v65 offset:9376
	s_waitcnt vmcnt(8)
	ds_write_b128 v55, v[112:115] offset:27712
	s_waitcnt lgkmcnt(3)
	v_mfma_f32_32x32x16_bf16 v[2:17], v[18:21], v[26:29], v[2:17]
	s_waitcnt lgkmcnt(1)
	v_mfma_f32_32x32x16_bf16 v[2:17], v[68:71], v[46:49], v[2:17]
	s_and_saveexec_b64 s[14:15], vcc
	s_cbranch_execz .LBB0_1112
	s_waitcnt vmcnt(7)
	ds_write_b128 v55, v[116:119] offset:36928
.LBB0_1112:
	s_or_b64 exec, exec, s[14:15]
	s_and_saveexec_b64 s[14:15], s[0:1]
	s_cbranch_execz .LBB0_1114
	s_waitcnt vmcnt(6)
	ds_write_b128 v57, v[120:123] offset:36928
.LBB0_1114:
	s_or_b64 exec, exec, s[14:15]
	s_waitcnt lgkmcnt(0)
	s_barrier
	ds_read_b128 v[42:45], v65 offset:36928
	ds_read_b128 v[46:49], v66 offset:27712
	s_waitcnt lgkmcnt(0)
	v_mfma_f32_32x32x16_bf16 v[2:17], v[42:45], v[46:49], v[2:17]
	ds_read_b128 v[42:45], v65 offset:36960
	ds_read_b128 v[46:49], v66 offset:27744
	s_waitcnt lgkmcnt(0)
	v_mfma_f32_32x32x16_bf16 v[2:17], v[42:45], v[46:49], v[2:17]
	ds_read_b128 v[42:45], v65 offset:36992
	ds_read_b128 v[46:49], v66 offset:27776
	s_waitcnt lgkmcnt(0)
	v_mfma_f32_32x32x16_bf16 v[2:17], v[42:45], v[46:49], v[2:17]
	ds_read_b128 v[42:45], v65 offset:37024
	ds_read_b128 v[46:49], v66 offset:27808
	s_waitcnt vmcnt(5)
	ds_write_b128 v55, v[124:127] offset:64
	s_waitcnt lgkmcnt(1)
	v_mfma_f32_32x32x16_bf16 v[2:17], v[42:45], v[46:49], v[2:17]
	s_and_saveexec_b64 s[14:15], vcc
	s_cbranch_execz .LBB0_1116
	s_waitcnt vmcnt(4)
	ds_write_b128 v55, v[128:131] offset:9280
.LBB0_1116:
	s_or_b64 exec, exec, s[14:15]
	s_and_saveexec_b64 s[14:15], s[0:1]
	s_cbranch_execz .LBB0_1118
	s_waitcnt vmcnt(3)
	ds_write_b128 v57, v[132:135] offset:9280
.LBB0_1118:
	s_or_b64 exec, exec, s[14:15]
	s_waitcnt lgkmcnt(0)
	s_barrier
	ds_read_b128 v[30:33], v65 offset:9280
	ds_read_b128 v[34:37], v66 offset:64
	s_waitcnt lgkmcnt(0)
	v_mfma_f32_32x32x16_bf16 v[2:17], v[30:33], v[34:37], v[2:17]
	ds_read_b128 v[30:33], v65 offset:9312
	ds_read_b128 v[34:37], v66 offset:96
	s_waitcnt lgkmcnt(0)
	v_mfma_f32_32x32x16_bf16 v[2:17], v[30:33], v[34:37], v[2:17]
	ds_read_b128 v[30:33], v65 offset:9344
	ds_read_b128 v[34:37], v66 offset:128
	s_waitcnt lgkmcnt(0)
	v_mfma_f32_32x32x16_bf16 v[2:17], v[30:33], v[34:37], v[2:17]
	ds_read_b128 v[30:33], v65 offset:9376
	ds_read_b128 v[34:37], v66 offset:160
	s_waitcnt vmcnt(2)
	ds_write_b128 v55, v[136:139] offset:27712
	s_waitcnt lgkmcnt(1)
	v_mfma_f32_32x32x16_bf16 v[2:17], v[30:33], v[34:37], v[2:17]
	s_and_saveexec_b64 s[14:15], vcc
	s_cbranch_execz .LBB0_1120
	s_waitcnt vmcnt(1)
	ds_write_b128 v55, v[140:143] offset:36928
.LBB0_1120:
	s_or_b64 exec, exec, s[14:15]
	s_and_saveexec_b64 s[14:15], s[0:1]
	s_cbranch_execz .LBB0_1122
	s_waitcnt vmcnt(0)
	ds_write_b128 v57, v[144:147] offset:36928

.LBB0_1270:
	s_or_b64 exec, exec, s[14:15]
	s_waitcnt vmcnt(0)
	v_ashrrev_i32_e32 v2, 6, v6
	v_lshrrev_b32_e32 v3, 30, v2
	v_add_u32_e32 v3, v2, v3
	v_ashrrev_i32_e32 v7, 2, v3
	v_mul_i32_i24_e32 v3, 4, v7
	v_and_b32_e32 v8, 31, v6
	v_sub_u32_e32 v2, v2, v3
	v_lshrrev_b32_e32 v3, 1, v6
	v_lshl_or_b32 v2, v2, 5, v8
	v_and_b32_e32 v6, 16, v3
	v_mul_lo_u32 v2, v2, s21
	v_add3_u32 v60, 0, v2, v6
	global_load_dwordx4 v[112:115], v[54:55], off offset:128
	global_load_dwordx4 v[116:119], v[50:51], off offset:128
	global_load_dwordx4 v[120:123], v[52:53], off offset:128
	global_load_dwordx4 v[124:127], v[54:55], off offset:256
	global_load_dwordx4 v[128:131], v[50:51], off offset:256
	global_load_dwordx4 v[132:135], v[52:53], off offset:256
	global_load_dwordx4 v[136:139], v[54:55], off offset:384
	global_load_dwordx4 v[140:143], v[50:51], off offset:384
	global_load_dwordx4 v[144:147], v[52:53], off offset:384
	s_waitcnt lgkmcnt(0)
	s_barrier
	global_load_dwordx4 v[100:103], v[54:55], off offset:512
	global_load_dwordx4 v[104:107], v[50:51], off offset:512
	global_load_dwordx4 v[108:111], v[52:53], off offset:512
	ds_read_b128 v[2:5], v60 offset:9280
	v_lshl_or_b32 v7, v7, 5, v8
	v_mul_lo_u32 v7, v7, s21
	v_add3_u32 v61, 0, v7, v6
	ds_read_b128 v[6:9], v61 offset:64
	ds_read_b128 v[18:21], v61 offset:96
	ds_read_b128 v[22:25], v60 offset:9312
	s_waitcnt lgkmcnt(2)
	v_mfma_f32_32x32x16_bf16 v[2:17], v[2:5], v[6:9], 0
	s_waitcnt lgkmcnt(0)
	v_mfma_f32_32x32x16_bf16 v[2:17], v[22:25], v[18:21], v[2:17]
	ds_read_b128 v[18:21], v60 offset:9344
	ds_read_b128 v[26:29], v61 offset:128
	ds_read_b128 v[42:45], v61 offset:160
	ds_read_b128 v[46:49], v60 offset:9376
	s_waitcnt lgkmcnt(2)
	v_mfma_f32_32x32x16_bf16 v[2:17], v[18:21], v[26:29], v[2:17]
	s_waitcnt vmcnt(11)
	ds_write_b128 v58, v[112:115] offset:27712
	s_waitcnt lgkmcnt(1)
	v_mfma_f32_32x32x16_bf16 v[2:17], v[46:49], v[42:45], v[2:17]
	s_and_saveexec_b64 s[14:15], vcc
	s_cbranch_execz .LBB0_1272
	s_waitcnt vmcnt(10)
	ds_write_b128 v58, v[116:119] offset:36928
.LBB0_1272:
	s_or_b64 exec, exec, s[14:15]
	s_and_saveexec_b64 s[14:15], s[0:1]
	s_cbranch_execz .LBB0_1274
	s_waitcnt vmcnt(9)
	ds_write_b128 v59, v[120:123] offset:36928
.LBB0_1274:
	s_or_b64 exec, exec, s[14:15]
	s_waitcnt lgkmcnt(0)
	s_barrier
	global_load_dwordx4 v[112:115], v[54:55], off offset:640
	global_load_dwordx4 v[116:119], v[50:51], off offset:640
	global_load_dwordx4 v[120:123], v[52:53], off offset:640
	ds_read_b128 v[30:33], v60 offset:36928
	ds_read_b128 v[34:37], v61 offset:27712
	ds_read_b128 v[38:41], v61 offset:27744
	ds_read_b128 v[42:45], v60 offset:36960
	s_waitcnt lgkmcnt(2)
	v_mfma_f32_32x32x16_bf16 v[2:17], v[30:33], v[34:37], v[2:17]
	s_waitcnt lgkmcnt(0)
	v_mfma_f32_32x32x16_bf16 v[2:17], v[42:45], v[38:41], v[2:17]
	ds_read_b128 v[30:33], v60 offset:36992
	ds_read_b128 v[38:41], v61 offset:27776
	ds_read_b128 v[42:45], v61 offset:27808
	ds_read_b128 v[46:49], v60 offset:37024
	s_waitcnt lgkmcnt(2)
	v_mfma_f32_32x32x16_bf16 v[2:17], v[30:33], v[38:41], v[2:17]
	s_waitcnt vmcnt(11)
	ds_write_b128 v58, v[124:127] offset:64
	s_waitcnt lgkmcnt(1)
	v_mfma_f32_32x32x16_bf16 v[2:17], v[46:49], v[42:45], v[2:17]
	s_and_saveexec_b64 s[14:15], vcc
	s_cbranch_execz .LBB0_1276
	s_waitcnt vmcnt(10)
	ds_write_b128 v58, v[128:131] offset:9280
.LBB0_1276:
	s_or_b64 exec, exec, s[14:15]
	s_and_saveexec_b64 s[14:15], s[0:1]
	s_cbranch_execz .LBB0_1278
	s_waitcnt vmcnt(9)
	ds_write_b128 v59, v[132:135] offset:9280
.LBB0_1278:
	s_or_b64 exec, exec, s[14:15]
	s_waitcnt lgkmcnt(0)
	s_barrier
	global_load_dwordx4 v[124:127], v[54:55], off offset:768
	global_load_dwordx4 v[128:131], v[50:51], off offset:768
	global_load_dwordx4 v[132:135], v[52:53], off offset:768
	ds_read_b128 v[18:21], v60 offset:9280
	ds_read_b128 v[22:25], v61 offset:64
	ds_read_b128 v[26:29], v61 offset:96
	ds_read_b128 v[42:45], v60 offset:9312
	s_waitcnt lgkmcnt(2)
	v_mfma_f32_32x32x16_bf16 v[2:17], v[18:21], v[22:25], v[2:17]
	ds_read_b128 v[18:21], v60 offset:9344
	ds_read_b128 v[22:25], v61 offset:128
	s_waitcnt lgkmcnt(2)
	v_mfma_f32_32x32x16_bf16 v[2:17], v[42:45], v[26:29], v[2:17]
	ds_read_b128 v[46:49], v61 offset:160
	ds_read_b128 v[62:65], v60 offset:9376
	s_waitcnt lgkmcnt(2)
	v_mfma_f32_32x32x16_bf16 v[2:17], v[18:21], v[22:25], v[2:17]
	s_waitcnt vmcnt(11)
	ds_write_b128 v58, v[136:139] offset:27712
	s_waitcnt lgkmcnt(1)
	v_mfma_f32_32x32x16_bf16 v[2:17], v[62:65], v[46:49], v[2:17]
	s_and_saveexec_b64 s[14:15], vcc
	s_cbranch_execz .LBB0_1280
	s_waitcnt vmcnt(10)
	ds_write_b128 v58, v[140:143] offset:36928
.LBB0_1280:
	s_or_b64 exec, exec, s[14:15]
	s_and_saveexec_b64 s[14:15], s[0:1]
	s_cbranch_execz .LBB0_1282
	s_waitcnt vmcnt(9)
	ds_write_b128 v59, v[144:147] offset:36928
.LBB0_1282:
	s_or_b64 exec, exec, s[14:15]
	s_waitcnt lgkmcnt(0)
	s_barrier
	global_load_dwordx4 v[136:139], v[54:55], off offset:896
	global_load_dwordx4 v[140:143], v[50:51], off offset:896
	global_load_dwordx4 v[144:147], v[52:53], off offset:896
	ds_read_b128 v[22:25], v60 offset:36928
	ds_read_b128 v[30:33], v61 offset:27712
	ds_read_b128 v[34:37], v61 offset:27744
	ds_read_b128 v[38:41], v60 offset:36960
	s_waitcnt lgkmcnt(2)
	v_mfma_f32_32x32x16_bf16 v[2:17], v[22:25], v[30:33], v[2:17]
	s_waitcnt lgkmcnt(0)
	v_mfma_f32_32x32x16_bf16 v[2:17], v[38:41], v[34:37], v[2:17]
	ds_read_b128 v[22:25], v60 offset:36992
	ds_read_b128 v[34:37], v61 offset:27776
	ds_read_b128 v[38:41], v61 offset:27808
	ds_read_b128 v[46:49], v60 offset:37024
	s_waitcnt lgkmcnt(2)
	v_mfma_f32_32x32x16_bf16 v[2:17], v[22:25], v[34:37], v[2:17]
	s_waitcnt vmcnt(11)
	ds_write_b128 v58, v[100:103] offset:64
	s_waitcnt lgkmcnt(1)
	v_mfma_f32_32x32x16_bf16 v[2:17], v[46:49], v[38:41], v[2:17]
	s_and_saveexec_b64 s[14:15], vcc
	s_cbranch_execz .LBB0_1284
	s_waitcnt vmcnt(10)
	ds_write_b128 v58, v[104:107] offset:9280
.LBB0_1284:
	s_or_b64 exec, exec, s[14:15]
	s_and_saveexec_b64 s[14:15], s[0:1]
	s_cbranch_execz .LBB0_1286
	s_waitcnt vmcnt(9)
	ds_write_b128 v59, v[108:111] offset:9280
.LBB0_1286:
	s_or_b64 exec, exec, s[14:15]
	s_waitcnt lgkmcnt(0)
	s_barrier
	global_load_dwordx4 v[100:103], v[54:55], off offset:1024
	global_load_dwordx4 v[104:107], v[50:51], off offset:1024
	global_load_dwordx4 v[108:111], v[52:53], off offset:1024
	ds_read_b128 v[18:21], v60 offset:9280
	ds_read_b128 v[26:29], v61 offset:64
	ds_read_b128 v[38:41], v61 offset:96
	ds_read_b128 v[42:45], v60 offset:9312
	s_waitcnt lgkmcnt(2)
	v_mfma_f32_32x32x16_bf16 v[2:17], v[18:21], v[26:29], v[2:17]
	s_waitcnt lgkmcnt(0)
	v_mfma_f32_32x32x16_bf16 v[2:17], v[42:45], v[38:41], v[2:17]
	ds_read_b128 v[18:21], v60 offset:9344
	ds_read_b128 v[38:41], v61 offset:128
	ds_read_b128 v[42:45], v61 offset:160
	ds_read_b128 v[46:49], v60 offset:9376
	s_waitcnt lgkmcnt(2)
	v_mfma_f32_32x32x16_bf16 v[2:17], v[18:21], v[38:41], v[2:17]
	s_waitcnt vmcnt(11)
	ds_write_b128 v58, v[112:115] offset:27712
	s_waitcnt lgkmcnt(1)
	v_mfma_f32_32x32x16_bf16 v[2:17], v[46:49], v[42:45], v[2:17]
	s_and_saveexec_b64 s[14:15], vcc
	s_cbranch_execz .LBB0_1288
	s_waitcnt vmcnt(10)
	ds_write_b128 v58, v[116:119] offset:36928

.LBB0_1290:
	s_or_b64 exec, exec, s[14:15]
	s_waitcnt lgkmcnt(0)
	s_barrier
	global_load_dwordx4 v[112:115], v[54:55], off offset:1152
	global_load_dwordx4 v[116:119], v[50:51], off offset:1152
	global_load_dwordx4 v[120:123], v[52:53], off offset:1152
	ds_read_b128 v[22:25], v60 offset:36928
	ds_read_b128 v[30:33], v61 offset:27712
	ds_read_b128 v[34:37], v61 offset:27744
	ds_read_b128 v[42:45], v60 offset:36960
	s_waitcnt lgkmcnt(2)
	v_mfma_f32_32x32x16_bf16 v[2:17], v[22:25], v[30:33], v[2:17]
	s_waitcnt lgkmcnt(0)
	v_mfma_f32_32x32x16_bf16 v[2:17], v[42:45], v[34:37], v[2:17]
	ds_read_b128 v[22:25], v60 offset:36992
	ds_read_b128 v[34:37], v61 offset:27776
	ds_read_b128 v[42:45], v61 offset:27808
	ds_read_b128 v[46:49], v60 offset:37024
	s_waitcnt lgkmcnt(2)
	v_mfma_f32_32x32x16_bf16 v[2:17], v[22:25], v[34:37], v[2:17]
	s_waitcnt vmcnt(11)
	ds_write_b128 v58, v[124:127] offset:64
	s_waitcnt lgkmcnt(1)
	v_mfma_f32_32x32x16_bf16 v[2:17], v[46:49], v[42:45], v[2:17]
	s_and_saveexec_b64 s[14:15], vcc
	s_cbranch_execz .LBB0_1292
	s_waitcnt vmcnt(10)
	ds_write_b128 v58, v[128:131] offset:9280

.LBB0_1294:
	s_or_b64 exec, exec, s[14:15]
	s_waitcnt lgkmcnt(0)
	s_barrier
	global_load_dwordx4 v[124:127], v[54:55], off offset:1280
	global_load_dwordx4 v[128:131], v[50:51], off offset:1280
	global_load_dwordx4 v[132:135], v[52:53], off offset:1280
	ds_read_b128 v[18:21], v60 offset:9280
	ds_read_b128 v[26:29], v61 offset:64
	ds_read_b128 v[38:41], v61 offset:96
	ds_read_b128 v[42:45], v60 offset:9312
	s_waitcnt lgkmcnt(2)
	v_mfma_f32_32x32x16_bf16 v[2:17], v[18:21], v[26:29], v[2:17]
	s_waitcnt lgkmcnt(0)
	v_mfma_f32_32x32x16_bf16 v[2:17], v[42:45], v[38:41], v[2:17]
	ds_read_b128 v[18:21], v60 offset:9344
	ds_read_b128 v[38:41], v61 offset:128
	ds_read_b128 v[42:45], v61 offset:160
	ds_read_b128 v[46:49], v60 offset:9376
	s_waitcnt lgkmcnt(2)
	v_mfma_f32_32x32x16_bf16 v[2:17], v[18:21], v[38:41], v[2:17]
	s_waitcnt vmcnt(11)
	ds_write_b128 v58, v[136:139] offset:27712
	s_waitcnt lgkmcnt(1)
	v_mfma_f32_32x32x16_bf16 v[2:17], v[46:49], v[42:45], v[2:17]
	s_and_saveexec_b64 s[14:15], vcc
	s_cbranch_execz .LBB0_1296
	s_waitcnt vmcnt(10)
	ds_write_b128 v58, v[140:143] offset:36928

.LBB0_1298:
	s_or_b64 exec, exec, s[14:15]
	s_waitcnt lgkmcnt(0)
	s_barrier
	global_load_dwordx4 v[136:139], v[54:55], off offset:1408
	global_load_dwordx4 v[140:143], v[50:51], off offset:1408
	global_load_dwordx4 v[144:147], v[52:53], off offset:1408
	ds_read_b128 v[22:25], v60 offset:36928
	ds_read_b128 v[30:33], v61 offset:27712
	ds_read_b128 v[34:37], v61 offset:27744
	ds_read_b128 v[42:45], v60 offset:36960
	s_waitcnt lgkmcnt(2)
	v_mfma_f32_32x32x16_bf16 v[2:17], v[22:25], v[30:33], v[2:17]
	s_waitcnt lgkmcnt(0)
	v_mfma_f32_32x32x16_bf16 v[2:17], v[42:45], v[34:37], v[2:17]
	ds_read_b128 v[22:25], v60 offset:36992
	ds_read_b128 v[34:37], v61 offset:27776
	ds_read_b128 v[42:45], v61 offset:27808
	ds_read_b128 v[46:49], v60 offset:37024
	s_waitcnt lgkmcnt(2)
	v_mfma_f32_32x32x16_bf16 v[2:17], v[22:25], v[34:37], v[2:17]
	s_waitcnt vmcnt(11)
	ds_write_b128 v58, v[100:103] offset:64
	s_waitcnt lgkmcnt(1)
	v_mfma_f32_32x32x16_bf16 v[2:17], v[46:49], v[42:45], v[2:17]
	s_and_saveexec_b64 s[14:15], vcc
	s_cbranch_execz .LBB0_1300
	s_waitcnt vmcnt(10)
	ds_write_b128 v58, v[104:107] offset:9280

.LBB0_1302:
	s_or_b64 exec, exec, s[14:15]
	s_waitcnt lgkmcnt(0)
	s_barrier
	global_load_dwordx4 v[100:103], v[54:55], off offset:1536
	global_load_dwordx4 v[104:107], v[50:51], off offset:1536
	global_load_dwordx4 v[108:111], v[52:53], off offset:1536
	ds_read_b128 v[18:21], v60 offset:9280
	ds_read_b128 v[26:29], v61 offset:64
	ds_read_b128 v[38:41], v61 offset:96
	ds_read_b128 v[42:45], v60 offset:9312
	s_waitcnt lgkmcnt(2)
	v_mfma_f32_32x32x16_bf16 v[2:17], v[18:21], v[26:29], v[2:17]
	s_waitcnt lgkmcnt(0)
	v_mfma_f32_32x32x16_bf16 v[2:17], v[42:45], v[38:41], v[2:17]
	ds_read_b128 v[18:21], v60 offset:9344
	ds_read_b128 v[38:41], v61 offset:128
	ds_read_b128 v[42:45], v61 offset:160
	ds_read_b128 v[46:49], v60 offset:9376
	s_waitcnt lgkmcnt(2)
	v_mfma_f32_32x32x16_bf16 v[2:17], v[18:21], v[38:41], v[2:17]
	s_waitcnt vmcnt(11)
	ds_write_b128 v58, v[112:115] offset:27712
	s_waitcnt lgkmcnt(1)
	v_mfma_f32_32x32x16_bf16 v[2:17], v[46:49], v[42:45], v[2:17]
	s_and_saveexec_b64 s[14:15], vcc
	s_cbranch_execz .LBB0_1304
	s_waitcnt vmcnt(10)
	ds_write_b128 v58, v[116:119] offset:36928

.LBB0_1306:
	s_or_b64 exec, exec, s[14:15]
	s_waitcnt lgkmcnt(0)
	s_barrier
	global_load_dwordx4 v[112:115], v[54:55], off offset:1664
	global_load_dwordx4 v[116:119], v[50:51], off offset:1664
	global_load_dwordx4 v[120:123], v[52:53], off offset:1664
	ds_read_b128 v[22:25], v60 offset:36928
	ds_read_b128 v[30:33], v61 offset:27712
	ds_read_b128 v[34:37], v61 offset:27744
	ds_read_b128 v[42:45], v60 offset:36960
	s_waitcnt lgkmcnt(2)
	v_mfma_f32_32x32x16_bf16 v[2:17], v[22:25], v[30:33], v[2:17]
	s_waitcnt lgkmcnt(0)
	v_mfma_f32_32x32x16_bf16 v[2:17], v[42:45], v[34:37], v[2:17]
	ds_read_b128 v[22:25], v60 offset:36992
	ds_read_b128 v[34:37], v61 offset:27776
	ds_read_b128 v[42:45], v61 offset:27808
	ds_read_b128 v[46:49], v60 offset:37024
	s_waitcnt lgkmcnt(2)
	v_mfma_f32_32x32x16_bf16 v[2:17], v[22:25], v[34:37], v[2:17]
	s_waitcnt vmcnt(11)
	ds_write_b128 v58, v[124:127] offset:64
	s_waitcnt lgkmcnt(1)
	v_mfma_f32_32x32x16_bf16 v[2:17], v[46:49], v[42:45], v[2:17]
	s_and_saveexec_b64 s[14:15], vcc
	s_cbranch_execz .LBB0_1308
	s_waitcnt vmcnt(10)
	ds_write_b128 v58, v[128:131] offset:9280

.LBB0_1310:
	s_or_b64 exec, exec, s[14:15]
	s_waitcnt lgkmcnt(0)
	s_barrier
	global_load_dwordx4 v[124:127], v[54:55], off offset:1792
	global_load_dwordx4 v[128:131], v[50:51], off offset:1792
	global_load_dwordx4 v[132:135], v[52:53], off offset:1792
	ds_read_b128 v[18:21], v60 offset:9280
	ds_read_b128 v[26:29], v61 offset:64
	ds_read_b128 v[38:41], v61 offset:96
	ds_read_b128 v[42:45], v60 offset:9312
	s_waitcnt lgkmcnt(2)
	v_mfma_f32_32x32x16_bf16 v[2:17], v[18:21], v[26:29], v[2:17]
	s_waitcnt lgkmcnt(0)
	v_mfma_f32_32x32x16_bf16 v[2:17], v[42:45], v[38:41], v[2:17]
	ds_read_b128 v[18:21], v60 offset:9344
	ds_read_b128 v[38:41], v61 offset:128
	ds_read_b128 v[42:45], v61 offset:160
	ds_read_b128 v[46:49], v60 offset:9376
	s_waitcnt lgkmcnt(2)
	v_mfma_f32_32x32x16_bf16 v[2:17], v[18:21], v[38:41], v[2:17]
	s_waitcnt vmcnt(11)
	ds_write_b128 v58, v[136:139] offset:27712
	s_waitcnt lgkmcnt(1)
	v_mfma_f32_32x32x16_bf16 v[2:17], v[46:49], v[42:45], v[2:17]
	s_and_saveexec_b64 s[14:15], vcc
	s_cbranch_execz .LBB0_1312
	s_waitcnt vmcnt(10)
	ds_write_b128 v58, v[140:143] offset:36928

.LBB0_1314:
	s_or_b64 exec, exec, s[14:15]
	s_waitcnt lgkmcnt(0)
	s_barrier
	global_load_dwordx4 v[136:139], v[54:55], off offset:1920
	global_load_dwordx4 v[140:143], v[50:51], off offset:1920
	global_load_dwordx4 v[144:147], v[52:53], off offset:1920
	ds_read_b128 v[22:25], v60 offset:36928
	ds_read_b128 v[30:33], v61 offset:27712
	ds_read_b128 v[34:37], v61 offset:27744
	ds_read_b128 v[42:45], v60 offset:36960
	s_waitcnt lgkmcnt(2)
	v_mfma_f32_32x32x16_bf16 v[2:17], v[22:25], v[30:33], v[2:17]
	ds_read_b128 v[22:25], v60 offset:36992
	ds_read_b128 v[30:33], v61 offset:27776
	s_waitcnt lgkmcnt(2)
	v_mfma_f32_32x32x16_bf16 v[2:17], v[42:45], v[34:37], v[2:17]
	ds_read_b128 v[34:37], v61 offset:27808
	ds_read_b128 v[62:65], v60 offset:37024
	s_waitcnt lgkmcnt(2)
	v_mfma_f32_32x32x16_bf16 v[2:17], v[22:25], v[30:33], v[2:17]
	s_waitcnt vmcnt(11)
	ds_write_b128 v58, v[100:103] offset:64
	s_waitcnt lgkmcnt(1)
	v_mfma_f32_32x32x16_bf16 v[2:17], v[62:65], v[34:37], v[2:17]
	s_and_saveexec_b64 s[14:15], vcc
	s_cbranch_execz .LBB0_1316
	s_waitcnt vmcnt(10)
	ds_write_b128 v58, v[104:107] offset:9280

.LBB0_1318:
	s_or_b64 exec, exec, s[14:15]
	s_waitcnt lgkmcnt(0)
	s_barrier
	ds_read_b128 v[18:21], v60 offset:9280
	ds_read_b128 v[26:29], v61 offset:64
	ds_read_b128 v[30:33], v61 offset:96
	ds_read_b128 v[34:37], v60 offset:9312
	s_waitcnt lgkmcnt(2)
	v_mfma_f32_32x32x16_bf16 v[2:17], v[18:21], v[26:29], v[2:17]
	ds_read_b128 v[18:21], v60 offset:9344
	ds_read_b128 v[26:29], v61 offset:128
	s_waitcnt lgkmcnt(2)
	v_mfma_f32_32x32x16_bf16 v[2:17], v[34:37], v[30:33], v[2:17]
	ds_read_b128 v[62:65], v61 offset:160
	ds_read_b128 v[66:69], v60 offset:9376
	s_waitcnt vmcnt(8)
	ds_write_b128 v58, v[112:115] offset:27712
	s_waitcnt lgkmcnt(3)
	v_mfma_f32_32x32x16_bf16 v[2:17], v[18:21], v[26:29], v[2:17]
	s_waitcnt lgkmcnt(1)
	v_mfma_f32_32x32x16_bf16 v[2:17], v[66:69], v[62:65], v[2:17]
	s_and_saveexec_b64 s[14:15], vcc
	s_cbranch_execz .LBB0_1320
	s_waitcnt vmcnt(7)
	ds_write_b128 v58, v[116:119] offset:36928
.LBB0_1320:
	s_or_b64 exec, exec, s[14:15]
	s_and_saveexec_b64 s[14:15], s[0:1]
	s_cbranch_execz .LBB0_1322
	s_waitcnt vmcnt(6)
	ds_write_b128 v59, v[120:123] offset:36928
.LBB0_1322:
	s_or_b64 exec, exec, s[14:15]
	s_waitcnt lgkmcnt(0)
	s_barrier
	ds_read_b128 v[42:45], v60 offset:36928
	ds_read_b128 v[46:49], v61 offset:27712
	s_waitcnt lgkmcnt(0)
	v_mfma_f32_32x32x16_bf16 v[2:17], v[42:45], v[46:49], v[2:17]
	ds_read_b128 v[42:45], v60 offset:36960
	ds_read_b128 v[46:49], v61 offset:27744
	s_waitcnt lgkmcnt(0)
	v_mfma_f32_32x32x16_bf16 v[2:17], v[42:45], v[46:49], v[2:17]
	ds_read_b128 v[42:45], v60 offset:36992
	ds_read_b128 v[46:49], v61 offset:27776
	s_waitcnt lgkmcnt(0)
	v_mfma_f32_32x32x16_bf16 v[2:17], v[42:45], v[46:49], v[2:17]
	ds_read_b128 v[42:45], v60 offset:37024
	ds_read_b128 v[46:49], v61 offset:27808
	s_waitcnt vmcnt(5)
	ds_write_b128 v58, v[124:127] offset:64
	s_waitcnt lgkmcnt(1)
	v_mfma_f32_32x32x16_bf16 v[2:17], v[42:45], v[46:49], v[2:17]
	s_and_saveexec_b64 s[14:15], vcc
	s_cbranch_execz .LBB0_1324
	s_waitcnt vmcnt(4)
	ds_write_b128 v58, v[128:131] offset:9280
.LBB0_1324:
	s_or_b64 exec, exec, s[14:15]
	s_and_saveexec_b64 s[14:15], s[0:1]
	s_cbranch_execz .LBB0_1326
	s_waitcnt vmcnt(3)
	ds_write_b128 v59, v[132:135] offset:9280
.LBB0_1326:
	s_or_b64 exec, exec, s[14:15]
	s_waitcnt lgkmcnt(0)
	s_barrier
	ds_read_b128 v[30:33], v60 offset:9280
	ds_read_b128 v[34:37], v61 offset:64
	s_waitcnt lgkmcnt(0)
	v_mfma_f32_32x32x16_bf16 v[2:17], v[30:33], v[34:37], v[2:17]
	ds_read_b128 v[30:33], v60 offset:9312
	ds_read_b128 v[34:37], v61 offset:96
	s_waitcnt lgkmcnt(0)
	v_mfma_f32_32x32x16_bf16 v[2:17], v[30:33], v[34:37], v[2:17]
	ds_read_b128 v[30:33], v60 offset:9344
	ds_read_b128 v[34:37], v61 offset:128
	s_waitcnt lgkmcnt(0)
	v_mfma_f32_32x32x16_bf16 v[2:17], v[30:33], v[34:37], v[2:17]
	ds_read_b128 v[30:33], v60 offset:9376
	ds_read_b128 v[34:37], v61 offset:160
	s_waitcnt vmcnt(2)
	ds_write_b128 v58, v[136:139] offset:27712
	s_waitcnt lgkmcnt(1)
	v_mfma_f32_32x32x16_bf16 v[2:17], v[30:33], v[34:37], v[2:17]
	s_and_saveexec_b64 s[14:15], vcc
	s_cbranch_execz .LBB0_1328
	s_waitcnt vmcnt(1)
	ds_write_b128 v58, v[140:143] offset:36928
.LBB0_1328:
	s_or_b64 exec, exec, s[14:15]
	s_and_saveexec_b64 s[14:15], s[0:1]
	s_cbranch_execz .LBB0_1330
	s_waitcnt vmcnt(0)
	ds_write_b128 v59, v[144:147] offset:36928

.LBB0_1646:
	s_or_b64 exec, exec, s[14:15]
	s_waitcnt vmcnt(0)
	v_ashrrev_i32_e32 v2, 6, v6
	v_lshrrev_b32_e32 v3, 30, v2
	v_add_u32_e32 v3, v2, v3
	v_ashrrev_i32_e32 v7, 2, v3
	v_mul_i32_i24_e32 v3, 4, v7
	v_and_b32_e32 v8, 31, v6
	v_sub_u32_e32 v2, v2, v3
	v_lshrrev_b32_e32 v3, 1, v6
	v_lshl_or_b32 v2, v2, 5, v8
	v_and_b32_e32 v6, 16, v3
	v_mul_lo_u32 v2, v2, s21
	v_add3_u32 v55, 0, v2, v6
	global_load_dwordx4 v[112:115], v[52:53], off offset:128
	global_load_dwordx4 v[116:119], v[48:49], off offset:128
	global_load_dwordx4 v[120:123], v[50:51], off offset:128
	global_load_dwordx4 v[124:127], v[52:53], off offset:256
	global_load_dwordx4 v[128:131], v[48:49], off offset:256
	global_load_dwordx4 v[132:135], v[50:51], off offset:256
	global_load_dwordx4 v[136:139], v[52:53], off offset:384
	global_load_dwordx4 v[140:143], v[48:49], off offset:384
	global_load_dwordx4 v[144:147], v[50:51], off offset:384
	s_waitcnt lgkmcnt(0)
	s_barrier
	global_load_dwordx4 v[100:103], v[52:53], off offset:512
	global_load_dwordx4 v[104:107], v[48:49], off offset:512
	global_load_dwordx4 v[108:111], v[50:51], off offset:512
	ds_read_b128 v[2:5], v55 offset:9280
	v_lshl_or_b32 v7, v7, 5, v8
	v_mul_lo_u32 v7, v7, s21
	v_add3_u32 v56, 0, v7, v6
	ds_read_b128 v[6:9], v56 offset:64
	ds_read_b128 v[18:21], v56 offset:96
	ds_read_b128 v[22:25], v55 offset:9312
	s_waitcnt lgkmcnt(2)
	v_mfma_f32_32x32x16_bf16 v[2:17], v[2:5], v[6:9], 0
	s_waitcnt lgkmcnt(0)
	v_mfma_f32_32x32x16_bf16 v[2:17], v[22:25], v[18:21], v[2:17]
	ds_read_b128 v[18:21], v55 offset:9344
	ds_read_b128 v[26:29], v56 offset:128
	ds_read_b128 v[42:45], v56 offset:160
	ds_read_b128 v[58:61], v55 offset:9376
	s_waitcnt lgkmcnt(2)
	v_mfma_f32_32x32x16_bf16 v[2:17], v[18:21], v[26:29], v[2:17]
	s_waitcnt vmcnt(11)
	ds_write_b128 v54, v[112:115] offset:27712
	s_waitcnt lgkmcnt(1)
	v_mfma_f32_32x32x16_bf16 v[2:17], v[58:61], v[42:45], v[2:17]
	s_and_saveexec_b64 s[14:15], vcc
	s_cbranch_execz .LBB0_1648
	s_waitcnt vmcnt(10)
	ds_write_b128 v54, v[116:119] offset:36928
.LBB0_1648:
	s_or_b64 exec, exec, s[14:15]
	s_and_saveexec_b64 s[14:15], s[0:1]
	s_cbranch_execz .LBB0_1650
	v_mad_u64_u32 v[34:35], s[48:49], v47, s21, v[46:47]
	s_waitcnt vmcnt(9)
	ds_write_b128 v34, v[120:123] offset:36928
.LBB0_1650:
	s_or_b64 exec, exec, s[14:15]
	s_waitcnt lgkmcnt(0)
	s_barrier
	global_load_dwordx4 v[112:115], v[52:53], off offset:640
	global_load_dwordx4 v[116:119], v[48:49], off offset:640
	global_load_dwordx4 v[120:123], v[50:51], off offset:640
	ds_read_b128 v[30:33], v55 offset:36928
	ds_read_b128 v[34:37], v56 offset:27712
	ds_read_b128 v[38:41], v56 offset:27744
	ds_read_b128 v[42:45], v55 offset:36960
	s_waitcnt lgkmcnt(2)
	v_mfma_f32_32x32x16_bf16 v[2:17], v[30:33], v[34:37], v[2:17]
	s_waitcnt lgkmcnt(0)
	v_mfma_f32_32x32x16_bf16 v[2:17], v[42:45], v[38:41], v[2:17]
	ds_read_b128 v[30:33], v55 offset:36992
	ds_read_b128 v[38:41], v56 offset:27776
	ds_read_b128 v[42:45], v56 offset:27808
	ds_read_b128 v[58:61], v55 offset:37024
	s_waitcnt lgkmcnt(2)
	v_mfma_f32_32x32x16_bf16 v[2:17], v[30:33], v[38:41], v[2:17]
	s_waitcnt vmcnt(11)
	ds_write_b128 v54, v[124:127] offset:64
	s_waitcnt lgkmcnt(1)
	v_mfma_f32_32x32x16_bf16 v[2:17], v[58:61], v[42:45], v[2:17]
	s_and_saveexec_b64 s[14:15], vcc
	s_cbranch_execz .LBB0_1652
	s_waitcnt vmcnt(10)
	ds_write_b128 v54, v[128:131] offset:9280
.LBB0_1652:
	s_or_b64 exec, exec, s[14:15]
	s_and_saveexec_b64 s[14:15], s[0:1]
	s_cbranch_execz .LBB0_1654
	v_mad_u64_u32 v[22:23], s[48:49], v47, s21, v[46:47]
	s_waitcnt vmcnt(9)
	ds_write_b128 v22, v[132:135] offset:9280
.LBB0_1654:
	s_or_b64 exec, exec, s[14:15]
	s_waitcnt lgkmcnt(0)
	s_barrier
	global_load_dwordx4 v[124:127], v[52:53], off offset:768
	global_load_dwordx4 v[128:131], v[48:49], off offset:768
	global_load_dwordx4 v[132:135], v[50:51], off offset:768
	ds_read_b128 v[18:21], v55 offset:9280
	ds_read_b128 v[22:25], v56 offset:64
	ds_read_b128 v[26:29], v56 offset:96
	ds_read_b128 v[42:45], v55 offset:9312
	s_waitcnt lgkmcnt(2)
	v_mfma_f32_32x32x16_bf16 v[2:17], v[18:21], v[22:25], v[2:17]
	ds_read_b128 v[18:21], v55 offset:9344
	ds_read_b128 v[22:25], v56 offset:128
	s_waitcnt lgkmcnt(2)
	v_mfma_f32_32x32x16_bf16 v[2:17], v[42:45], v[26:29], v[2:17]
	ds_read_b128 v[58:61], v56 offset:160
	ds_read_b128 v[68:71], v55 offset:9376
	s_waitcnt lgkmcnt(2)
	v_mfma_f32_32x32x16_bf16 v[2:17], v[18:21], v[22:25], v[2:17]
	s_waitcnt vmcnt(11)
	ds_write_b128 v54, v[136:139] offset:27712
	s_waitcnt lgkmcnt(1)
	v_mfma_f32_32x32x16_bf16 v[2:17], v[68:71], v[58:61], v[2:17]
	s_and_saveexec_b64 s[14:15], vcc
	s_cbranch_execz .LBB0_1656
	s_waitcnt vmcnt(10)
	ds_write_b128 v54, v[140:143] offset:36928
.LBB0_1656:
	s_or_b64 exec, exec, s[14:15]
	s_and_saveexec_b64 s[14:15], s[0:1]
	s_cbranch_execz .LBB0_1658
	v_mad_u64_u32 v[22:23], s[48:49], v47, s21, v[46:47]
	s_waitcnt vmcnt(9)
	ds_write_b128 v22, v[144:147] offset:36928
.LBB0_1658:
	s_or_b64 exec, exec, s[14:15]
	s_waitcnt lgkmcnt(0)
	s_barrier
	global_load_dwordx4 v[136:139], v[52:53], off offset:896
	global_load_dwordx4 v[140:143], v[48:49], off offset:896
	global_load_dwordx4 v[144:147], v[50:51], off offset:896
	ds_read_b128 v[22:25], v55 offset:36928
	ds_read_b128 v[30:33], v56 offset:27712
	ds_read_b128 v[34:37], v56 offset:27744
	ds_read_b128 v[38:41], v55 offset:36960
	s_waitcnt lgkmcnt(2)
	v_mfma_f32_32x32x16_bf16 v[2:17], v[22:25], v[30:33], v[2:17]
	s_waitcnt lgkmcnt(0)
	v_mfma_f32_32x32x16_bf16 v[2:17], v[38:41], v[34:37], v[2:17]
	ds_read_b128 v[22:25], v55 offset:36992
	ds_read_b128 v[34:37], v56 offset:27776
	ds_read_b128 v[38:41], v56 offset:27808
	ds_read_b128 v[58:61], v55 offset:37024
	s_waitcnt lgkmcnt(2)
	v_mfma_f32_32x32x16_bf16 v[2:17], v[22:25], v[34:37], v[2:17]
	s_waitcnt vmcnt(11)
	ds_write_b128 v54, v[100:103] offset:64
	s_waitcnt lgkmcnt(1)
	v_mfma_f32_32x32x16_bf16 v[2:17], v[58:61], v[38:41], v[2:17]
	s_and_saveexec_b64 s[14:15], vcc
	s_cbranch_execz .LBB0_1660
	s_waitcnt vmcnt(10)
	ds_write_b128 v54, v[104:107] offset:9280
.LBB0_1660:
	s_or_b64 exec, exec, s[14:15]
	s_and_saveexec_b64 s[14:15], s[0:1]
	s_cbranch_execz .LBB0_1662
	v_mad_u64_u32 v[26:27], s[48:49], v47, s21, v[46:47]
	s_waitcnt vmcnt(9)
	ds_write_b128 v26, v[108:111] offset:9280
.LBB0_1662:
	s_or_b64 exec, exec, s[14:15]
	s_waitcnt lgkmcnt(0)
	s_barrier
	global_load_dwordx4 v[100:103], v[52:53], off offset:1024
	global_load_dwordx4 v[104:107], v[48:49], off offset:1024
	global_load_dwordx4 v[108:111], v[50:51], off offset:1024
	ds_read_b128 v[18:21], v55 offset:9280
	ds_read_b128 v[26:29], v56 offset:64
	ds_read_b128 v[38:41], v56 offset:96
	ds_read_b128 v[42:45], v55 offset:9312
	s_waitcnt lgkmcnt(2)
	v_mfma_f32_32x32x16_bf16 v[2:17], v[18:21], v[26:29], v[2:17]
	s_waitcnt lgkmcnt(0)
	v_mfma_f32_32x32x16_bf16 v[2:17], v[42:45], v[38:41], v[2:17]
	ds_read_b128 v[18:21], v55 offset:9344
	ds_read_b128 v[38:41], v56 offset:128
	ds_read_b128 v[42:45], v56 offset:160
	ds_read_b128 v[58:61], v55 offset:9376
	s_waitcnt lgkmcnt(2)
	v_mfma_f32_32x32x16_bf16 v[2:17], v[18:21], v[38:41], v[2:17]
	s_waitcnt vmcnt(11)
	ds_write_b128 v54, v[112:115] offset:27712
	s_waitcnt lgkmcnt(1)
	v_mfma_f32_32x32x16_bf16 v[2:17], v[58:61], v[42:45], v[2:17]
	s_and_saveexec_b64 s[14:15], vcc
	s_cbranch_execz .LBB0_1664
	s_waitcnt vmcnt(10)
	ds_write_b128 v54, v[116:119] offset:36928
.LBB0_1664:
	s_or_b64 exec, exec, s[14:15]
	s_and_saveexec_b64 s[14:15], s[0:1]
	s_cbranch_execz .LBB0_1666
	v_mad_u64_u32 v[30:31], s[48:49], v47, s21, v[46:47]
	s_waitcnt vmcnt(9)
	ds_write_b128 v30, v[120:123] offset:36928
.LBB0_1666:
	s_or_b64 exec, exec, s[14:15]
	s_waitcnt lgkmcnt(0)
	s_barrier
	global_load_dwordx4 v[112:115], v[52:53], off offset:1152
	global_load_dwordx4 v[116:119], v[48:49], off offset:1152
	global_load_dwordx4 v[120:123], v[50:51], off offset:1152
	ds_read_b128 v[22:25], v55 offset:36928
	ds_read_b128 v[30:33], v56 offset:27712
	ds_read_b128 v[34:37], v56 offset:27744
	ds_read_b128 v[42:45], v55 offset:36960
	s_waitcnt lgkmcnt(2)
	v_mfma_f32_32x32x16_bf16 v[2:17], v[22:25], v[30:33], v[2:17]
	s_waitcnt lgkmcnt(0)
	v_mfma_f32_32x32x16_bf16 v[2:17], v[42:45], v[34:37], v[2:17]
	ds_read_b128 v[22:25], v55 offset:36992
	ds_read_b128 v[34:37], v56 offset:27776
	ds_read_b128 v[42:45], v56 offset:27808
	ds_read_b128 v[58:61], v55 offset:37024
	s_waitcnt lgkmcnt(2)
	v_mfma_f32_32x32x16_bf16 v[2:17], v[22:25], v[34:37], v[2:17]
	s_waitcnt vmcnt(11)
	ds_write_b128 v54, v[124:127] offset:64
	s_waitcnt lgkmcnt(1)
	v_mfma_f32_32x32x16_bf16 v[2:17], v[58:61], v[42:45], v[2:17]
	s_and_saveexec_b64 s[14:15], vcc
	s_cbranch_execz .LBB0_1668
	s_waitcnt vmcnt(10)
	ds_write_b128 v54, v[128:131] offset:9280
.LBB0_1668:
	s_or_b64 exec, exec, s[14:15]
	s_and_saveexec_b64 s[14:15], s[0:1]
	s_cbranch_execz .LBB0_1670
	v_mad_u64_u32 v[26:27], s[48:49], v47, s21, v[46:47]
	s_waitcnt vmcnt(9)
	ds_write_b128 v26, v[132:135] offset:9280
.LBB0_1670:
	s_or_b64 exec, exec, s[14:15]
	s_waitcnt lgkmcnt(0)
	s_barrier
	global_load_dwordx4 v[124:127], v[52:53], off offset:1280
	global_load_dwordx4 v[128:131], v[48:49], off offset:1280
	global_load_dwordx4 v[132:135], v[50:51], off offset:1280
	ds_read_b128 v[18:21], v55 offset:9280
	ds_read_b128 v[26:29], v56 offset:64
	ds_read_b128 v[38:41], v56 offset:96
	ds_read_b128 v[42:45], v55 offset:9312
	s_waitcnt lgkmcnt(2)
	v_mfma_f32_32x32x16_bf16 v[2:17], v[18:21], v[26:29], v[2:17]
	s_waitcnt lgkmcnt(0)
	v_mfma_f32_32x32x16_bf16 v[2:17], v[42:45], v[38:41], v[2:17]
	ds_read_b128 v[18:21], v55 offset:9344
	ds_read_b128 v[38:41], v56 offset:128
	ds_read_b128 v[42:45], v56 offset:160
	ds_read_b128 v[58:61], v55 offset:9376
	s_waitcnt lgkmcnt(2)
	v_mfma_f32_32x32x16_bf16 v[2:17], v[18:21], v[38:41], v[2:17]
	s_waitcnt vmcnt(11)
	ds_write_b128 v54, v[136:139] offset:27712
	s_waitcnt lgkmcnt(1)
	v_mfma_f32_32x32x16_bf16 v[2:17], v[58:61], v[42:45], v[2:17]
	s_and_saveexec_b64 s[14:15], vcc
	s_cbranch_execz .LBB0_1672
	s_waitcnt vmcnt(10)
	ds_write_b128 v54, v[140:143] offset:36928
.LBB0_1672:
	s_or_b64 exec, exec, s[14:15]
	s_and_saveexec_b64 s[14:15], s[0:1]
	s_cbranch_execz .LBB0_1674
	v_mad_u64_u32 v[30:31], s[48:49], v47, s21, v[46:47]
	s_waitcnt vmcnt(9)
	ds_write_b128 v30, v[144:147] offset:36928
.LBB0_1674:
	s_or_b64 exec, exec, s[14:15]
	s_waitcnt lgkmcnt(0)
	s_barrier
	global_load_dwordx4 v[136:139], v[52:53], off offset:1408
	global_load_dwordx4 v[140:143], v[48:49], off offset:1408
	global_load_dwordx4 v[144:147], v[50:51], off offset:1408
	ds_read_b128 v[22:25], v55 offset:36928
	ds_read_b128 v[30:33], v56 offset:27712
	ds_read_b128 v[34:37], v56 offset:27744
	ds_read_b128 v[42:45], v55 offset:36960
	s_waitcnt lgkmcnt(2)
	v_mfma_f32_32x32x16_bf16 v[2:17], v[22:25], v[30:33], v[2:17]
	s_waitcnt lgkmcnt(0)
	v_mfma_f32_32x32x16_bf16 v[2:17], v[42:45], v[34:37], v[2:17]
	ds_read_b128 v[22:25], v55 offset:36992
	ds_read_b128 v[34:37], v56 offset:27776
	ds_read_b128 v[42:45], v56 offset:27808
	ds_read_b128 v[58:61], v55 offset:37024
	s_waitcnt lgkmcnt(2)
	v_mfma_f32_32x32x16_bf16 v[2:17], v[22:25], v[34:37], v[2:17]
	s_waitcnt vmcnt(11)
	ds_write_b128 v54, v[100:103] offset:64
	s_waitcnt lgkmcnt(1)
	v_mfma_f32_32x32x16_bf16 v[2:17], v[58:61], v[42:45], v[2:17]
	s_and_saveexec_b64 s[14:15], vcc
	s_cbranch_execz .LBB0_1676
	s_waitcnt vmcnt(10)
	ds_write_b128 v54, v[104:107] offset:9280

.LBB0_1678:
	s_or_b64 exec, exec, s[14:15]
	s_waitcnt lgkmcnt(0)
	s_barrier
	global_load_dwordx4 v[100:103], v[52:53], off offset:1536
	global_load_dwordx4 v[104:107], v[48:49], off offset:1536
	global_load_dwordx4 v[108:111], v[50:51], off offset:1536
	ds_read_b128 v[18:21], v55 offset:9280
	ds_read_b128 v[26:29], v56 offset:64
	ds_read_b128 v[38:41], v56 offset:96
	ds_read_b128 v[42:45], v55 offset:9312
	s_waitcnt lgkmcnt(2)
	v_mfma_f32_32x32x16_bf16 v[2:17], v[18:21], v[26:29], v[2:17]
	s_waitcnt lgkmcnt(0)
	v_mfma_f32_32x32x16_bf16 v[2:17], v[42:45], v[38:41], v[2:17]
	ds_read_b128 v[18:21], v55 offset:9344
	ds_read_b128 v[38:41], v56 offset:128
	ds_read_b128 v[42:45], v56 offset:160
	ds_read_b128 v[58:61], v55 offset:9376
	s_waitcnt lgkmcnt(2)
	v_mfma_f32_32x32x16_bf16 v[2:17], v[18:21], v[38:41], v[2:17]
	s_waitcnt vmcnt(11)
	ds_write_b128 v54, v[112:115] offset:27712
	s_waitcnt lgkmcnt(1)
	v_mfma_f32_32x32x16_bf16 v[2:17], v[58:61], v[42:45], v[2:17]
	s_and_saveexec_b64 s[14:15], vcc
	s_cbranch_execz .LBB0_1680
	s_waitcnt vmcnt(10)
	ds_write_b128 v54, v[116:119] offset:36928

.LBB0_1682:
	s_or_b64 exec, exec, s[14:15]
	s_waitcnt lgkmcnt(0)
	s_barrier
	global_load_dwordx4 v[112:115], v[52:53], off offset:1664
	global_load_dwordx4 v[116:119], v[48:49], off offset:1664
	global_load_dwordx4 v[120:123], v[50:51], off offset:1664
	ds_read_b128 v[22:25], v55 offset:36928
	ds_read_b128 v[30:33], v56 offset:27712
	ds_read_b128 v[34:37], v56 offset:27744
	ds_read_b128 v[42:45], v55 offset:36960
	s_waitcnt lgkmcnt(2)
	v_mfma_f32_32x32x16_bf16 v[2:17], v[22:25], v[30:33], v[2:17]
	s_waitcnt lgkmcnt(0)
	v_mfma_f32_32x32x16_bf16 v[2:17], v[42:45], v[34:37], v[2:17]
	ds_read_b128 v[22:25], v55 offset:36992
	ds_read_b128 v[34:37], v56 offset:27776
	ds_read_b128 v[42:45], v56 offset:27808
	ds_read_b128 v[58:61], v55 offset:37024
	s_waitcnt lgkmcnt(2)
	v_mfma_f32_32x32x16_bf16 v[2:17], v[22:25], v[34:37], v[2:17]
	s_waitcnt vmcnt(11)
	ds_write_b128 v54, v[124:127] offset:64
	s_waitcnt lgkmcnt(1)
	v_mfma_f32_32x32x16_bf16 v[2:17], v[58:61], v[42:45], v[2:17]
	s_and_saveexec_b64 s[14:15], vcc
	s_cbranch_execz .LBB0_1684
	s_waitcnt vmcnt(10)
	ds_write_b128 v54, v[128:131] offset:9280

.LBB0_1686:
	s_or_b64 exec, exec, s[14:15]
	s_waitcnt lgkmcnt(0)
	s_barrier
	global_load_dwordx4 v[124:127], v[52:53], off offset:1792
	global_load_dwordx4 v[128:131], v[48:49], off offset:1792
	global_load_dwordx4 v[132:135], v[50:51], off offset:1792
	ds_read_b128 v[18:21], v55 offset:9280
	ds_read_b128 v[26:29], v56 offset:64
	ds_read_b128 v[38:41], v56 offset:96
	ds_read_b128 v[42:45], v55 offset:9312
	s_waitcnt lgkmcnt(2)
	v_mfma_f32_32x32x16_bf16 v[2:17], v[18:21], v[26:29], v[2:17]
	s_waitcnt lgkmcnt(0)
	v_mfma_f32_32x32x16_bf16 v[2:17], v[42:45], v[38:41], v[2:17]
	ds_read_b128 v[18:21], v55 offset:9344
	ds_read_b128 v[38:41], v56 offset:128
	ds_read_b128 v[42:45], v56 offset:160
	ds_read_b128 v[58:61], v55 offset:9376
	s_waitcnt lgkmcnt(2)
	v_mfma_f32_32x32x16_bf16 v[2:17], v[18:21], v[38:41], v[2:17]
	s_waitcnt vmcnt(11)
	ds_write_b128 v54, v[136:139] offset:27712
	s_waitcnt lgkmcnt(1)
	v_mfma_f32_32x32x16_bf16 v[2:17], v[58:61], v[42:45], v[2:17]
	s_and_saveexec_b64 s[14:15], vcc
	s_cbranch_execz .LBB0_1688
	s_waitcnt vmcnt(10)
	ds_write_b128 v54, v[140:143] offset:36928

.LBB0_1690:
	s_or_b64 exec, exec, s[14:15]
	s_waitcnt lgkmcnt(0)
	s_barrier
	global_load_dwordx4 v[136:139], v[52:53], off offset:1920
	global_load_dwordx4 v[140:143], v[48:49], off offset:1920
	global_load_dwordx4 v[144:147], v[50:51], off offset:1920
	ds_read_b128 v[22:25], v55 offset:36928
	ds_read_b128 v[30:33], v56 offset:27712
	ds_read_b128 v[34:37], v56 offset:27744
	ds_read_b128 v[42:45], v55 offset:36960
	s_waitcnt lgkmcnt(2)
	v_mfma_f32_32x32x16_bf16 v[2:17], v[22:25], v[30:33], v[2:17]
	s_waitcnt lgkmcnt(0)
	v_mfma_f32_32x32x16_bf16 v[2:17], v[42:45], v[34:37], v[2:17]
	ds_read_b128 v[22:25], v55 offset:36992
	ds_read_b128 v[34:37], v56 offset:27776
	ds_read_b128 v[58:61], v56 offset:27808
	ds_read_b128 v[68:71], v55 offset:37024
	s_waitcnt lgkmcnt(2)
	v_mfma_f32_32x32x16_bf16 v[2:17], v[22:25], v[34:37], v[2:17]
	s_waitcnt vmcnt(11)
	ds_write_b128 v54, v[100:103] offset:64
	s_waitcnt lgkmcnt(1)
	v_mfma_f32_32x32x16_bf16 v[2:17], v[68:71], v[58:61], v[2:17]
	s_and_saveexec_b64 s[14:15], vcc
	s_cbranch_execz .LBB0_1692
	s_waitcnt vmcnt(10)
	ds_write_b128 v54, v[104:107] offset:9280

.LBB0_1694:
	s_or_b64 exec, exec, s[14:15]
	s_waitcnt lgkmcnt(0)
	s_barrier
	ds_read_b128 v[18:21], v55 offset:9280
	ds_read_b128 v[26:29], v56 offset:64
	ds_read_b128 v[34:37], v56 offset:96
	ds_read_b128 v[38:41], v55 offset:9312
	s_waitcnt lgkmcnt(2)
	v_mfma_f32_32x32x16_bf16 v[2:17], v[18:21], v[26:29], v[2:17]
	ds_read_b128 v[18:21], v55 offset:9344
	ds_read_b128 v[26:29], v56 offset:128
	s_waitcnt lgkmcnt(2)
	v_mfma_f32_32x32x16_bf16 v[2:17], v[38:41], v[34:37], v[2:17]
	ds_read_b128 v[58:61], v56 offset:160
	ds_read_b128 v[68:71], v55 offset:9376
	s_waitcnt lgkmcnt(2)
	v_mfma_f32_32x32x16_bf16 v[2:17], v[18:21], v[26:29], v[2:17]
	s_waitcnt vmcnt(8)
	ds_write_b128 v54, v[112:115] offset:27712
	s_waitcnt lgkmcnt(1)
	v_mfma_f32_32x32x16_bf16 v[2:17], v[68:71], v[58:61], v[2:17]
	s_and_saveexec_b64 s[14:15], vcc
	s_cbranch_execz .LBB0_1696
	s_waitcnt vmcnt(7)
	ds_write_b128 v54, v[116:119] offset:36928
.LBB0_1696:
	s_or_b64 exec, exec, s[14:15]
	s_and_saveexec_b64 s[14:15], s[0:1]
	s_cbranch_execz .LBB0_1698
	v_mad_u64_u32 v[18:19], s[48:49], v47, s21, v[46:47]
	s_waitcnt vmcnt(6)
	ds_write_b128 v18, v[120:123] offset:36928
.LBB0_1698:
	s_or_b64 exec, exec, s[14:15]
	s_waitcnt lgkmcnt(0)
	s_barrier
	ds_read_b128 v[42:45], v55 offset:36928
	ds_read_b128 v[48:51], v56 offset:27712
	s_waitcnt lgkmcnt(0)
	v_mfma_f32_32x32x16_bf16 v[2:17], v[42:45], v[48:51], v[2:17]
	ds_read_b128 v[42:45], v55 offset:36960
	ds_read_b128 v[48:51], v56 offset:27744
	s_waitcnt lgkmcnt(0)
	v_mfma_f32_32x32x16_bf16 v[2:17], v[42:45], v[48:51], v[2:17]
	ds_read_b128 v[42:45], v55 offset:36992
	ds_read_b128 v[48:51], v56 offset:27776
	s_waitcnt lgkmcnt(0)
	v_mfma_f32_32x32x16_bf16 v[2:17], v[42:45], v[48:51], v[2:17]
	ds_read_b128 v[42:45], v55 offset:37024
	ds_read_b128 v[48:51], v56 offset:27808
	s_waitcnt vmcnt(5)
	ds_write_b128 v54, v[124:127] offset:64
	s_waitcnt lgkmcnt(1)
	v_mfma_f32_32x32x16_bf16 v[2:17], v[42:45], v[48:51], v[2:17]
	s_and_saveexec_b64 s[14:15], vcc
	s_cbranch_execz .LBB0_1700
	s_waitcnt vmcnt(4)
	ds_write_b128 v54, v[128:131] offset:9280
.LBB0_1700:
	s_or_b64 exec, exec, s[14:15]
	s_and_saveexec_b64 s[14:15], s[0:1]
	s_cbranch_execz .LBB0_1702
	v_mad_u64_u32 v[34:35], s[48:49], v47, s21, v[46:47]
	s_waitcnt vmcnt(3)
	ds_write_b128 v34, v[132:135] offset:9280
.LBB0_1702:
	s_or_b64 exec, exec, s[14:15]
	s_waitcnt lgkmcnt(0)
	s_barrier
	ds_read_b128 v[26:29], v55 offset:9280
	ds_read_b128 v[34:37], v56 offset:64
	s_waitcnt lgkmcnt(0)
	v_mfma_f32_32x32x16_bf16 v[2:17], v[26:29], v[34:37], v[2:17]
	ds_read_b128 v[26:29], v55 offset:9312
	ds_read_b128 v[34:37], v56 offset:96
	s_waitcnt lgkmcnt(0)
	v_mfma_f32_32x32x16_bf16 v[2:17], v[26:29], v[34:37], v[2:17]
	ds_read_b128 v[26:29], v55 offset:9344
	ds_read_b128 v[34:37], v56 offset:128
	s_waitcnt lgkmcnt(0)
	v_mfma_f32_32x32x16_bf16 v[2:17], v[26:29], v[34:37], v[2:17]
	ds_read_b128 v[26:29], v55 offset:9376
	ds_read_b128 v[34:37], v56 offset:160
	s_waitcnt vmcnt(2)
	ds_write_b128 v54, v[136:139] offset:27712
	s_waitcnt lgkmcnt(1)
	v_mfma_f32_32x32x16_bf16 v[2:17], v[26:29], v[34:37], v[2:17]
	s_and_saveexec_b64 s[14:15], vcc
	s_cbranch_execz .LBB0_1704
	s_waitcnt vmcnt(1)
	ds_write_b128 v54, v[140:143] offset:36928
.LBB0_1704:
	s_or_b64 exec, exec, s[14:15]
	s_and_saveexec_b64 s[14:15], s[0:1]
	s_cbranch_execz .LBB0_1706
	v_mad_u64_u32 v[22:23], s[0:1], v47, s21, v[46:47]
	s_waitcnt vmcnt(0)
	ds_write_b128 v22, v[144:147] offset:36928

.LBB0_1710:
	s_or_b64 exec, exec, s[14:15]
	s_waitcnt vmcnt(0)
	v_ashrrev_i32_e32 v18, 6, v22
	v_lshrrev_b32_e32 v19, 30, v18
	v_add_u32_e32 v19, v18, v19
	v_ashrrev_i32_e32 v23, 2, v19
	v_mul_i32_i24_e32 v19, 4, v23
	v_and_b32_e32 v24, 31, v22
	v_sub_u32_e32 v18, v18, v19
	v_lshrrev_b32_e32 v19, 1, v22
	v_lshl_or_b32 v18, v18, 5, v24
	v_and_b32_e32 v22, 16, v19
	v_mul_lo_u32 v18, v18, s21
	v_add3_u32 v67, 0, v18, v22
	global_load_dwordx4 v[112:115], v[74:75], off offset:128
	global_load_dwordx4 v[116:119], v[70:71], off offset:128
	global_load_dwordx4 v[120:123], v[72:73], off offset:128
	global_load_dwordx4 v[124:127], v[74:75], off offset:256
	global_load_dwordx4 v[128:131], v[70:71], off offset:256
	global_load_dwordx4 v[132:135], v[72:73], off offset:256
	global_load_dwordx4 v[136:139], v[74:75], off offset:384
	global_load_dwordx4 v[140:143], v[70:71], off offset:384
	global_load_dwordx4 v[144:147], v[72:73], off offset:384
	s_waitcnt lgkmcnt(0)
	s_barrier
	global_load_dwordx4 v[100:103], v[74:75], off offset:512
	global_load_dwordx4 v[104:107], v[70:71], off offset:512
	global_load_dwordx4 v[108:111], v[72:73], off offset:512
	ds_read_b128 v[18:21], v67 offset:9280
	v_lshl_or_b32 v23, v23, 5, v24
	v_mul_lo_u32 v23, v23, s21
	v_add3_u32 v69, 0, v23, v22
	ds_read_b128 v[22:25], v69 offset:64
	ds_read_b128 v[34:37], v69 offset:96
	ds_read_b128 v[38:41], v67 offset:9312
	s_waitcnt lgkmcnt(2)
	v_mfma_f32_32x32x16_bf16 v[18:33], v[18:21], v[22:25], 0
	s_waitcnt lgkmcnt(0)
	v_mfma_f32_32x32x16_bf16 v[18:33], v[38:41], v[34:37], v[18:33]
	ds_read_b128 v[34:37], v67 offset:9344
	ds_read_b128 v[42:45], v69 offset:128
	ds_read_b128 v[58:61], v69 offset:160
	ds_read_b128 v[78:81], v67 offset:9376
	s_waitcnt lgkmcnt(2)
	v_mfma_f32_32x32x16_bf16 v[18:33], v[34:37], v[42:45], v[18:33]
	s_waitcnt vmcnt(11)
	ds_write_b128 v76, v[112:115] offset:27712
	s_waitcnt lgkmcnt(1)
	v_mfma_f32_32x32x16_bf16 v[18:33], v[78:81], v[58:61], v[18:33]
	s_and_saveexec_b64 s[14:15], vcc
	s_cbranch_execz .LBB0_1712
	s_waitcnt vmcnt(10)
	ds_write_b128 v76, v[116:119] offset:36928
.LBB0_1712:
	s_or_b64 exec, exec, s[14:15]
	s_and_saveexec_b64 s[14:15], s[0:1]
	s_cbranch_execz .LBB0_1714
	v_mad_u64_u32 v[50:51], s[30:31], v65, s21, v[68:69]
	s_waitcnt vmcnt(9)
	ds_write_b128 v50, v[120:123] offset:36928
.LBB0_1714:
	s_or_b64 exec, exec, s[14:15]
	s_waitcnt lgkmcnt(0)
	s_barrier
	global_load_dwordx4 v[112:115], v[74:75], off offset:640
	global_load_dwordx4 v[116:119], v[70:71], off offset:640
	global_load_dwordx4 v[120:123], v[72:73], off offset:640
	ds_read_b128 v[46:49], v67 offset:36928
	ds_read_b128 v[50:53], v69 offset:27712
	ds_read_b128 v[54:57], v69 offset:27744
	ds_read_b128 v[58:61], v67 offset:36960
	s_waitcnt lgkmcnt(2)
	v_mfma_f32_32x32x16_bf16 v[18:33], v[46:49], v[50:53], v[18:33]
	s_waitcnt lgkmcnt(0)
	v_mfma_f32_32x32x16_bf16 v[18:33], v[58:61], v[54:57], v[18:33]
	ds_read_b128 v[46:49], v67 offset:36992
	ds_read_b128 v[54:57], v69 offset:27776
	ds_read_b128 v[58:61], v69 offset:27808
	ds_read_b128 v[78:81], v67 offset:37024
	s_waitcnt lgkmcnt(2)
	v_mfma_f32_32x32x16_bf16 v[18:33], v[46:49], v[54:57], v[18:33]
	s_waitcnt vmcnt(11)
	ds_write_b128 v76, v[124:127] offset:64
	s_waitcnt lgkmcnt(1)
	v_mfma_f32_32x32x16_bf16 v[18:33], v[78:81], v[58:61], v[18:33]
	s_and_saveexec_b64 s[14:15], vcc
	s_cbranch_execz .LBB0_1716
	s_waitcnt vmcnt(10)
	ds_write_b128 v76, v[128:131] offset:9280
.LBB0_1716:
	s_or_b64 exec, exec, s[14:15]
	s_and_saveexec_b64 s[14:15], s[0:1]
	s_cbranch_execz .LBB0_1718
	v_mad_u64_u32 v[38:39], s[30:31], v65, s21, v[68:69]
	s_waitcnt vmcnt(9)
	ds_write_b128 v38, v[132:135] offset:9280
.LBB0_1718:
	s_or_b64 exec, exec, s[14:15]
	s_waitcnt lgkmcnt(0)
	s_barrier
	global_load_dwordx4 v[124:127], v[74:75], off offset:768
	global_load_dwordx4 v[128:131], v[70:71], off offset:768
	global_load_dwordx4 v[132:135], v[72:73], off offset:768
	ds_read_b128 v[34:37], v67 offset:9280
	ds_read_b128 v[38:41], v69 offset:64
	ds_read_b128 v[42:45], v69 offset:96
	ds_read_b128 v[58:61], v67 offset:9312
	s_waitcnt lgkmcnt(2)
	v_mfma_f32_32x32x16_bf16 v[18:33], v[34:37], v[38:41], v[18:33]
	ds_read_b128 v[34:37], v67 offset:9344
	ds_read_b128 v[38:41], v69 offset:128
	s_waitcnt lgkmcnt(2)
	v_mfma_f32_32x32x16_bf16 v[18:33], v[58:61], v[42:45], v[18:33]
	ds_read_b128 v[78:81], v69 offset:160
	ds_read_b128 v[82:85], v67 offset:9376
	s_waitcnt lgkmcnt(2)
	v_mfma_f32_32x32x16_bf16 v[18:33], v[34:37], v[38:41], v[18:33]
	s_waitcnt vmcnt(11)
	ds_write_b128 v76, v[136:139] offset:27712
	s_waitcnt lgkmcnt(1)
	v_mfma_f32_32x32x16_bf16 v[18:33], v[82:85], v[78:81], v[18:33]
	s_and_saveexec_b64 s[14:15], vcc
	s_cbranch_execz .LBB0_1720
	s_waitcnt vmcnt(10)
	ds_write_b128 v76, v[140:143] offset:36928
.LBB0_1720:
	s_or_b64 exec, exec, s[14:15]
	s_and_saveexec_b64 s[14:15], s[0:1]
	s_cbranch_execz .LBB0_1722
	v_mad_u64_u32 v[38:39], s[30:31], v65, s21, v[68:69]
	s_waitcnt vmcnt(9)
	ds_write_b128 v38, v[144:147] offset:36928
.LBB0_1722:
	s_or_b64 exec, exec, s[14:15]
	s_waitcnt lgkmcnt(0)
	s_barrier
	global_load_dwordx4 v[136:139], v[74:75], off offset:896
	global_load_dwordx4 v[140:143], v[70:71], off offset:896
	global_load_dwordx4 v[144:147], v[72:73], off offset:896
	ds_read_b128 v[38:41], v67 offset:36928
	ds_read_b128 v[46:49], v69 offset:27712
	ds_read_b128 v[50:53], v69 offset:27744
	ds_read_b128 v[54:57], v67 offset:36960
	s_waitcnt lgkmcnt(2)
	v_mfma_f32_32x32x16_bf16 v[18:33], v[38:41], v[46:49], v[18:33]
	s_waitcnt lgkmcnt(0)
	v_mfma_f32_32x32x16_bf16 v[18:33], v[54:57], v[50:53], v[18:33]
	ds_read_b128 v[38:41], v67 offset:36992
	ds_read_b128 v[50:53], v69 offset:27776
	ds_read_b128 v[54:57], v69 offset:27808
	ds_read_b128 v[78:81], v67 offset:37024
	s_waitcnt lgkmcnt(2)
	v_mfma_f32_32x32x16_bf16 v[18:33], v[38:41], v[50:53], v[18:33]
	s_waitcnt vmcnt(11)
	ds_write_b128 v76, v[100:103] offset:64
	s_waitcnt lgkmcnt(1)
	v_mfma_f32_32x32x16_bf16 v[18:33], v[78:81], v[54:57], v[18:33]
	s_and_saveexec_b64 s[14:15], vcc
	s_cbranch_execz .LBB0_1724
	s_waitcnt vmcnt(10)
	ds_write_b128 v76, v[104:107] offset:9280
.LBB0_1724:
	s_or_b64 exec, exec, s[14:15]
	s_and_saveexec_b64 s[14:15], s[0:1]
	s_cbranch_execz .LBB0_1726
	v_mad_u64_u32 v[42:43], s[30:31], v65, s21, v[68:69]
	s_waitcnt vmcnt(9)
	ds_write_b128 v42, v[108:111] offset:9280
.LBB0_1726:
	s_or_b64 exec, exec, s[14:15]
	s_waitcnt lgkmcnt(0)
	s_barrier
	global_load_dwordx4 v[100:103], v[74:75], off offset:1024
	global_load_dwordx4 v[104:107], v[70:71], off offset:1024
	global_load_dwordx4 v[108:111], v[72:73], off offset:1024
	ds_read_b128 v[34:37], v67 offset:9280
	ds_read_b128 v[42:45], v69 offset:64
	ds_read_b128 v[54:57], v69 offset:96
	ds_read_b128 v[58:61], v67 offset:9312
	s_waitcnt lgkmcnt(2)
	v_mfma_f32_32x32x16_bf16 v[18:33], v[34:37], v[42:45], v[18:33]
	s_waitcnt lgkmcnt(0)
	v_mfma_f32_32x32x16_bf16 v[18:33], v[58:61], v[54:57], v[18:33]
	ds_read_b128 v[34:37], v67 offset:9344
	ds_read_b128 v[54:57], v69 offset:128
	ds_read_b128 v[58:61], v69 offset:160
	ds_read_b128 v[78:81], v67 offset:9376
	s_waitcnt lgkmcnt(2)
	v_mfma_f32_32x32x16_bf16 v[18:33], v[34:37], v[54:57], v[18:33]
	s_waitcnt vmcnt(11)
	ds_write_b128 v76, v[112:115] offset:27712
	s_waitcnt lgkmcnt(1)
	v_mfma_f32_32x32x16_bf16 v[18:33], v[78:81], v[58:61], v[18:33]
	s_and_saveexec_b64 s[14:15], vcc
	s_cbranch_execz .LBB0_1728
	s_waitcnt vmcnt(10)
	ds_write_b128 v76, v[116:119] offset:36928
.LBB0_1728:
	s_or_b64 exec, exec, s[14:15]
	s_and_saveexec_b64 s[14:15], s[0:1]
	s_cbranch_execz .LBB0_1730
	v_mad_u64_u32 v[46:47], s[30:31], v65, s21, v[68:69]
	s_waitcnt vmcnt(9)
	ds_write_b128 v46, v[120:123] offset:36928
.LBB0_1730:
	s_or_b64 exec, exec, s[14:15]
	s_waitcnt lgkmcnt(0)
	s_barrier
	global_load_dwordx4 v[112:115], v[74:75], off offset:1152
	global_load_dwordx4 v[116:119], v[70:71], off offset:1152
	global_load_dwordx4 v[120:123], v[72:73], off offset:1152
	ds_read_b128 v[38:41], v67 offset:36928
	ds_read_b128 v[46:49], v69 offset:27712
	ds_read_b128 v[50:53], v69 offset:27744
	ds_read_b128 v[58:61], v67 offset:36960
	s_waitcnt lgkmcnt(2)
	v_mfma_f32_32x32x16_bf16 v[18:33], v[38:41], v[46:49], v[18:33]
	s_waitcnt lgkmcnt(0)
	v_mfma_f32_32x32x16_bf16 v[18:33], v[58:61], v[50:53], v[18:33]
	ds_read_b128 v[38:41], v67 offset:36992
	ds_read_b128 v[50:53], v69 offset:27776
	ds_read_b128 v[58:61], v69 offset:27808
	ds_read_b128 v[78:81], v67 offset:37024
	s_waitcnt lgkmcnt(2)
	v_mfma_f32_32x32x16_bf16 v[18:33], v[38:41], v[50:53], v[18:33]
	s_waitcnt vmcnt(11)
	ds_write_b128 v76, v[124:127] offset:64
	s_waitcnt lgkmcnt(1)
	v_mfma_f32_32x32x16_bf16 v[18:33], v[78:81], v[58:61], v[18:33]
	s_and_saveexec_b64 s[14:15], vcc
	s_cbranch_execz .LBB0_1732
	s_waitcnt vmcnt(10)
	ds_write_b128 v76, v[128:131] offset:9280
.LBB0_1732:
	s_or_b64 exec, exec, s[14:15]
	s_and_saveexec_b64 s[14:15], s[0:1]
	s_cbranch_execz .LBB0_1734
	v_mad_u64_u32 v[42:43], s[30:31], v65, s21, v[68:69]
	s_waitcnt vmcnt(9)
	ds_write_b128 v42, v[132:135] offset:9280
.LBB0_1734:
	s_or_b64 exec, exec, s[14:15]
	s_waitcnt lgkmcnt(0)
	s_barrier
	global_load_dwordx4 v[124:127], v[74:75], off offset:1280
	global_load_dwordx4 v[128:131], v[70:71], off offset:1280
	global_load_dwordx4 v[132:135], v[72:73], off offset:1280
	ds_read_b128 v[34:37], v67 offset:9280
	ds_read_b128 v[42:45], v69 offset:64
	ds_read_b128 v[54:57], v69 offset:96
	ds_read_b128 v[58:61], v67 offset:9312
	s_waitcnt lgkmcnt(2)
	v_mfma_f32_32x32x16_bf16 v[18:33], v[34:37], v[42:45], v[18:33]
	s_waitcnt lgkmcnt(0)
	v_mfma_f32_32x32x16_bf16 v[18:33], v[58:61], v[54:57], v[18:33]
	ds_read_b128 v[34:37], v67 offset:9344
	ds_read_b128 v[54:57], v69 offset:128
	ds_read_b128 v[58:61], v69 offset:160
	ds_read_b128 v[78:81], v67 offset:9376
	s_waitcnt lgkmcnt(2)
	v_mfma_f32_32x32x16_bf16 v[18:33], v[34:37], v[54:57], v[18:33]
	s_waitcnt vmcnt(11)
	ds_write_b128 v76, v[136:139] offset:27712
	s_waitcnt lgkmcnt(1)
	v_mfma_f32_32x32x16_bf16 v[18:33], v[78:81], v[58:61], v[18:33]
	s_and_saveexec_b64 s[14:15], vcc
	s_cbranch_execz .LBB0_1736
	s_waitcnt vmcnt(10)
	ds_write_b128 v76, v[140:143] offset:36928
.LBB0_1736:
	s_or_b64 exec, exec, s[14:15]
	s_and_saveexec_b64 s[14:15], s[0:1]
	s_cbranch_execz .LBB0_1738
	v_mad_u64_u32 v[46:47], s[30:31], v65, s21, v[68:69]
	s_waitcnt vmcnt(9)
	ds_write_b128 v46, v[144:147] offset:36928
.LBB0_1738:
	s_or_b64 exec, exec, s[14:15]
	s_waitcnt lgkmcnt(0)
	s_barrier
	global_load_dwordx4 v[136:139], v[74:75], off offset:1408
	global_load_dwordx4 v[140:143], v[70:71], off offset:1408
	global_load_dwordx4 v[144:147], v[72:73], off offset:1408
	ds_read_b128 v[38:41], v67 offset:36928
	ds_read_b128 v[46:49], v69 offset:27712
	ds_read_b128 v[50:53], v69 offset:27744
	ds_read_b128 v[58:61], v67 offset:36960
	s_waitcnt lgkmcnt(2)
	v_mfma_f32_32x32x16_bf16 v[18:33], v[38:41], v[46:49], v[18:33]
	s_waitcnt lgkmcnt(0)
	v_mfma_f32_32x32x16_bf16 v[18:33], v[58:61], v[50:53], v[18:33]
	ds_read_b128 v[38:41], v67 offset:36992
	ds_read_b128 v[50:53], v69 offset:27776
	ds_read_b128 v[58:61], v69 offset:27808
	ds_read_b128 v[78:81], v67 offset:37024
	s_waitcnt lgkmcnt(2)
	v_mfma_f32_32x32x16_bf16 v[18:33], v[38:41], v[50:53], v[18:33]
	s_waitcnt vmcnt(11)
	ds_write_b128 v76, v[100:103] offset:64
	s_waitcnt lgkmcnt(1)
	v_mfma_f32_32x32x16_bf16 v[18:33], v[78:81], v[58:61], v[18:33]
	s_and_saveexec_b64 s[14:15], vcc
	s_cbranch_execz .LBB0_1740
	s_waitcnt vmcnt(10)
	ds_write_b128 v76, v[104:107] offset:9280

.LBB0_1742:
	s_or_b64 exec, exec, s[14:15]
	s_waitcnt lgkmcnt(0)
	s_barrier
	global_load_dwordx4 v[100:103], v[74:75], off offset:1536
	global_load_dwordx4 v[104:107], v[70:71], off offset:1536
	global_load_dwordx4 v[108:111], v[72:73], off offset:1536
	ds_read_b128 v[34:37], v67 offset:9280
	ds_read_b128 v[42:45], v69 offset:64
	ds_read_b128 v[54:57], v69 offset:96
	ds_read_b128 v[58:61], v67 offset:9312
	s_waitcnt lgkmcnt(2)
	v_mfma_f32_32x32x16_bf16 v[18:33], v[34:37], v[42:45], v[18:33]
	s_waitcnt lgkmcnt(0)
	v_mfma_f32_32x32x16_bf16 v[18:33], v[58:61], v[54:57], v[18:33]
	ds_read_b128 v[34:37], v67 offset:9344
	ds_read_b128 v[54:57], v69 offset:128
	ds_read_b128 v[58:61], v69 offset:160
	ds_read_b128 v[78:81], v67 offset:9376
	s_waitcnt lgkmcnt(2)
	v_mfma_f32_32x32x16_bf16 v[18:33], v[34:37], v[54:57], v[18:33]
	s_waitcnt vmcnt(11)
	ds_write_b128 v76, v[112:115] offset:27712
	s_waitcnt lgkmcnt(1)
	v_mfma_f32_32x32x16_bf16 v[18:33], v[78:81], v[58:61], v[18:33]
	s_and_saveexec_b64 s[14:15], vcc
	s_cbranch_execz .LBB0_1744
	s_waitcnt vmcnt(10)
	ds_write_b128 v76, v[116:119] offset:36928

.LBB0_1746:
	s_or_b64 exec, exec, s[14:15]
	s_waitcnt lgkmcnt(0)
	s_barrier
	global_load_dwordx4 v[112:115], v[74:75], off offset:1664
	global_load_dwordx4 v[116:119], v[70:71], off offset:1664
	global_load_dwordx4 v[120:123], v[72:73], off offset:1664
	ds_read_b128 v[38:41], v67 offset:36928
	ds_read_b128 v[46:49], v69 offset:27712
	ds_read_b128 v[50:53], v69 offset:27744
	ds_read_b128 v[58:61], v67 offset:36960
	s_waitcnt lgkmcnt(2)
	v_mfma_f32_32x32x16_bf16 v[18:33], v[38:41], v[46:49], v[18:33]
	s_waitcnt lgkmcnt(0)
	v_mfma_f32_32x32x16_bf16 v[18:33], v[58:61], v[50:53], v[18:33]
	ds_read_b128 v[38:41], v67 offset:36992
	ds_read_b128 v[50:53], v69 offset:27776
	ds_read_b128 v[58:61], v69 offset:27808
	ds_read_b128 v[78:81], v67 offset:37024
	s_waitcnt lgkmcnt(2)
	v_mfma_f32_32x32x16_bf16 v[18:33], v[38:41], v[50:53], v[18:33]
	s_waitcnt vmcnt(11)
	ds_write_b128 v76, v[124:127] offset:64
	s_waitcnt lgkmcnt(1)
	v_mfma_f32_32x32x16_bf16 v[18:33], v[78:81], v[58:61], v[18:33]
	s_and_saveexec_b64 s[14:15], vcc
	s_cbranch_execz .LBB0_1748
	s_waitcnt vmcnt(10)
	ds_write_b128 v76, v[128:131] offset:9280

.LBB0_1750:
	s_or_b64 exec, exec, s[14:15]
	s_waitcnt lgkmcnt(0)
	s_barrier
	global_load_dwordx4 v[124:127], v[74:75], off offset:1792
	global_load_dwordx4 v[128:131], v[70:71], off offset:1792
	global_load_dwordx4 v[132:135], v[72:73], off offset:1792
	ds_read_b128 v[34:37], v67 offset:9280
	ds_read_b128 v[42:45], v69 offset:64
	ds_read_b128 v[54:57], v69 offset:96
	ds_read_b128 v[58:61], v67 offset:9312
	s_waitcnt lgkmcnt(2)
	v_mfma_f32_32x32x16_bf16 v[18:33], v[34:37], v[42:45], v[18:33]
	s_waitcnt lgkmcnt(0)
	v_mfma_f32_32x32x16_bf16 v[18:33], v[58:61], v[54:57], v[18:33]
	ds_read_b128 v[34:37], v67 offset:9344
	ds_read_b128 v[54:57], v69 offset:128
	ds_read_b128 v[58:61], v69 offset:160
	ds_read_b128 v[78:81], v67 offset:9376
	s_waitcnt lgkmcnt(2)
	v_mfma_f32_32x32x16_bf16 v[18:33], v[34:37], v[54:57], v[18:33]
	s_waitcnt vmcnt(11)
	ds_write_b128 v76, v[136:139] offset:27712
	s_waitcnt lgkmcnt(1)
	v_mfma_f32_32x32x16_bf16 v[18:33], v[78:81], v[58:61], v[18:33]
	s_and_saveexec_b64 s[14:15], vcc
	s_cbranch_execz .LBB0_1752
	s_waitcnt vmcnt(10)
	ds_write_b128 v76, v[140:143] offset:36928

.LBB0_1754:
	s_or_b64 exec, exec, s[14:15]
	s_waitcnt lgkmcnt(0)
	s_barrier
	global_load_dwordx4 v[136:139], v[74:75], off offset:1920
	global_load_dwordx4 v[140:143], v[70:71], off offset:1920
	global_load_dwordx4 v[144:147], v[72:73], off offset:1920
	ds_read_b128 v[38:41], v67 offset:36928
	ds_read_b128 v[46:49], v69 offset:27712
	ds_read_b128 v[50:53], v69 offset:27744
	ds_read_b128 v[58:61], v67 offset:36960
	s_waitcnt lgkmcnt(2)
	v_mfma_f32_32x32x16_bf16 v[18:33], v[38:41], v[46:49], v[18:33]
	s_waitcnt lgkmcnt(0)
	v_mfma_f32_32x32x16_bf16 v[18:33], v[58:61], v[50:53], v[18:33]
	ds_read_b128 v[38:41], v67 offset:36992
	ds_read_b128 v[50:53], v69 offset:27776
	ds_read_b128 v[78:81], v69 offset:27808
	ds_read_b128 v[82:85], v67 offset:37024
	s_waitcnt lgkmcnt(2)
	v_mfma_f32_32x32x16_bf16 v[18:33], v[38:41], v[50:53], v[18:33]
	s_waitcnt vmcnt(11)
	ds_write_b128 v76, v[100:103] offset:64
	s_waitcnt lgkmcnt(1)
	v_mfma_f32_32x32x16_bf16 v[18:33], v[82:85], v[78:81], v[18:33]
	s_and_saveexec_b64 s[14:15], vcc
	s_cbranch_execz .LBB0_1756
	s_waitcnt vmcnt(10)
	ds_write_b128 v76, v[104:107] offset:9280

.LBB0_1758:
	s_or_b64 exec, exec, s[14:15]
	s_waitcnt lgkmcnt(0)
	s_barrier
	ds_read_b128 v[34:37], v67 offset:9280
	ds_read_b128 v[42:45], v69 offset:64
	ds_read_b128 v[50:53], v69 offset:96
	ds_read_b128 v[54:57], v67 offset:9312
	s_waitcnt lgkmcnt(2)
	v_mfma_f32_32x32x16_bf16 v[18:33], v[34:37], v[42:45], v[18:33]
	ds_read_b128 v[34:37], v67 offset:9344
	ds_read_b128 v[42:45], v69 offset:128
	s_waitcnt lgkmcnt(2)
	v_mfma_f32_32x32x16_bf16 v[18:33], v[54:57], v[50:53], v[18:33]
	ds_read_b128 v[78:81], v69 offset:160
	ds_read_b128 v[82:85], v67 offset:9376
	s_waitcnt lgkmcnt(2)
	v_mfma_f32_32x32x16_bf16 v[18:33], v[34:37], v[42:45], v[18:33]
	s_waitcnt vmcnt(8)
	ds_write_b128 v76, v[112:115] offset:27712
	s_waitcnt lgkmcnt(1)
	v_mfma_f32_32x32x16_bf16 v[18:33], v[82:85], v[78:81], v[18:33]
	s_and_saveexec_b64 s[14:15], vcc
	s_cbranch_execz .LBB0_1760
	s_waitcnt vmcnt(7)
	ds_write_b128 v76, v[116:119] offset:36928
.LBB0_1760:
	s_or_b64 exec, exec, s[14:15]
	s_and_saveexec_b64 s[14:15], s[0:1]
	s_cbranch_execz .LBB0_1762
	v_mad_u64_u32 v[34:35], s[30:31], v65, s21, v[68:69]
	s_waitcnt vmcnt(6)
	ds_write_b128 v34, v[120:123] offset:36928
.LBB0_1762:
	s_or_b64 exec, exec, s[14:15]
	s_waitcnt lgkmcnt(0)
	s_barrier
	ds_read_b128 v[58:61], v67 offset:36928
	ds_read_b128 v[70:73], v69 offset:27712
	s_waitcnt lgkmcnt(0)
	v_mfma_f32_32x32x16_bf16 v[18:33], v[58:61], v[70:73], v[18:33]
	ds_read_b128 v[58:61], v67 offset:36960
	ds_read_b128 v[70:73], v69 offset:27744
	s_waitcnt lgkmcnt(0)
	v_mfma_f32_32x32x16_bf16 v[18:33], v[58:61], v[70:73], v[18:33]
	ds_read_b128 v[58:61], v67 offset:36992
	ds_read_b128 v[70:73], v69 offset:27776
	s_waitcnt lgkmcnt(0)
	v_mfma_f32_32x32x16_bf16 v[18:33], v[58:61], v[70:73], v[18:33]
	ds_read_b128 v[58:61], v67 offset:37024
	ds_read_b128 v[70:73], v69 offset:27808
	s_waitcnt vmcnt(5)
	ds_write_b128 v76, v[124:127] offset:64
	s_waitcnt lgkmcnt(1)
	v_mfma_f32_32x32x16_bf16 v[18:33], v[58:61], v[70:73], v[18:33]
	s_and_saveexec_b64 s[14:15], vcc
	s_cbranch_execz .LBB0_1764
	s_waitcnt vmcnt(4)
	ds_write_b128 v76, v[128:131] offset:9280
.LBB0_1764:
	s_or_b64 exec, exec, s[14:15]
	s_and_saveexec_b64 s[14:15], s[0:1]
	s_cbranch_execz .LBB0_1766
	v_mad_u64_u32 v[50:51], s[30:31], v65, s21, v[68:69]
	s_waitcnt vmcnt(3)
	ds_write_b128 v50, v[132:135] offset:9280
.LBB0_1766:
	s_or_b64 exec, exec, s[14:15]
	s_waitcnt lgkmcnt(0)
	s_barrier
	ds_read_b128 v[42:45], v67 offset:9280
	ds_read_b128 v[50:53], v69 offset:64
	s_waitcnt lgkmcnt(0)
	v_mfma_f32_32x32x16_bf16 v[18:33], v[42:45], v[50:53], v[18:33]
	ds_read_b128 v[42:45], v67 offset:9312
	ds_read_b128 v[50:53], v69 offset:96
	s_waitcnt lgkmcnt(0)
	v_mfma_f32_32x32x16_bf16 v[18:33], v[42:45], v[50:53], v[18:33]
	ds_read_b128 v[42:45], v67 offset:9344
	ds_read_b128 v[50:53], v69 offset:128
	s_waitcnt lgkmcnt(0)
	v_mfma_f32_32x32x16_bf16 v[18:33], v[42:45], v[50:53], v[18:33]
	ds_read_b128 v[42:45], v67 offset:9376
	ds_read_b128 v[50:53], v69 offset:160
	s_waitcnt vmcnt(2)
	ds_write_b128 v76, v[136:139] offset:27712
	s_waitcnt lgkmcnt(1)
	v_mfma_f32_32x32x16_bf16 v[18:33], v[42:45], v[50:53], v[18:33]
	s_and_saveexec_b64 s[14:15], vcc
	s_cbranch_execz .LBB0_1768
	s_waitcnt vmcnt(1)
	ds_write_b128 v76, v[140:143] offset:36928
.LBB0_1768:
	s_or_b64 exec, exec, s[14:15]
	s_and_saveexec_b64 s[14:15], s[0:1]
	s_cbranch_execz .LBB0_1641
	v_mad_u64_u32 v[38:39], s[0:1], v65, s21, v[68:69]
	s_waitcnt vmcnt(0)
	ds_write_b128 v38, v[144:147] offset:36928
	s_branch .LBB0_1641

.LBB0_1854:
	s_or_b64 exec, exec, s[14:15]
	s_waitcnt vmcnt(0)
	v_ashrrev_i32_e32 v2, 6, v8
	v_lshrrev_b32_e32 v3, 30, v2
	s_mov_b64 s[14:15], 0x400000
	v_add_u32_e32 v3, v2, v3
	v_lshl_add_u64 v[60:61], v[6:7], 0, s[14:15]
	v_ashrrev_i32_e32 v6, 2, v3
	v_mul_i32_i24_e32 v3, 4, v6
	v_and_b32_e32 v7, 31, v8
	v_sub_u32_e32 v2, v2, v3
	v_lshrrev_b32_e32 v3, 1, v8
	v_lshl_or_b32 v2, v2, 5, v7
	v_and_b32_e32 v8, 16, v3
	v_mul_lo_u32 v2, v2, s21
	v_add3_u32 v53, 0, v2, v8
	global_load_dwordx4 v[112:115], v[60:61], off offset:128
	global_load_dwordx4 v[116:119], v[56:57], off offset:128
	global_load_dwordx4 v[120:123], v[58:59], off offset:128
	global_load_dwordx4 v[124:127], v[60:61], off offset:256
	global_load_dwordx4 v[128:131], v[56:57], off offset:256
	global_load_dwordx4 v[132:135], v[58:59], off offset:256
	global_load_dwordx4 v[136:139], v[60:61], off offset:384
	global_load_dwordx4 v[140:143], v[56:57], off offset:384
	global_load_dwordx4 v[144:147], v[58:59], off offset:384
	s_waitcnt lgkmcnt(0)
	s_barrier
	global_load_dwordx4 v[100:103], v[60:61], off offset:512
	global_load_dwordx4 v[104:107], v[56:57], off offset:512
	global_load_dwordx4 v[108:111], v[58:59], off offset:512
	ds_read_b128 v[2:5], v53 offset:9280
	v_lshl_or_b32 v6, v6, 5, v7
	v_mul_lo_u32 v6, v6, s21
	v_add3_u32 v55, 0, v6, v8
	ds_read_b128 v[6:9], v55 offset:64
	ds_read_b128 v[18:21], v55 offset:96
	ds_read_b128 v[22:25], v53 offset:9312
	s_waitcnt lgkmcnt(2)
	v_mfma_f32_32x32x16_bf16 v[2:17], v[2:5], v[6:9], 0
	s_waitcnt lgkmcnt(0)
	v_mfma_f32_32x32x16_bf16 v[2:17], v[22:25], v[18:21], v[2:17]
	ds_read_b128 v[18:21], v53 offset:9344
	ds_read_b128 v[26:29], v55 offset:128
	ds_read_b128 v[42:45], v55 offset:160
	ds_read_b128 v[46:49], v53 offset:9376
	s_waitcnt lgkmcnt(2)
	v_mfma_f32_32x32x16_bf16 v[2:17], v[18:21], v[26:29], v[2:17]
	s_waitcnt vmcnt(11)
	ds_write_b128 v62, v[112:115] offset:27712
	s_waitcnt lgkmcnt(1)
	v_mfma_f32_32x32x16_bf16 v[2:17], v[46:49], v[42:45], v[2:17]
	s_and_saveexec_b64 s[14:15], vcc
	s_cbranch_execz .LBB0_1856
	s_waitcnt vmcnt(10)
	ds_write_b128 v62, v[116:119] offset:36928
.LBB0_1856:
	s_or_b64 exec, exec, s[14:15]
	s_and_saveexec_b64 s[14:15], s[0:1]
	s_cbranch_execz .LBB0_1858
	s_waitcnt vmcnt(9)
	ds_write_b128 v63, v[120:123] offset:36928
.LBB0_1858:
	s_or_b64 exec, exec, s[14:15]
	s_waitcnt lgkmcnt(0)
	s_barrier
	global_load_dwordx4 v[112:115], v[60:61], off offset:640
	global_load_dwordx4 v[116:119], v[56:57], off offset:640
	global_load_dwordx4 v[120:123], v[58:59], off offset:640
	ds_read_b128 v[30:33], v53 offset:36928
	ds_read_b128 v[34:37], v55 offset:27712
	ds_read_b128 v[38:41], v55 offset:27744
	ds_read_b128 v[42:45], v53 offset:36960
	s_waitcnt lgkmcnt(2)
	v_mfma_f32_32x32x16_bf16 v[2:17], v[30:33], v[34:37], v[2:17]
	s_waitcnt lgkmcnt(0)
	v_mfma_f32_32x32x16_bf16 v[2:17], v[42:45], v[38:41], v[2:17]
	ds_read_b128 v[30:33], v53 offset:36992
	ds_read_b128 v[38:41], v55 offset:27776
	ds_read_b128 v[42:45], v55 offset:27808
	ds_read_b128 v[46:49], v53 offset:37024
	s_waitcnt lgkmcnt(2)
	v_mfma_f32_32x32x16_bf16 v[2:17], v[30:33], v[38:41], v[2:17]
	s_waitcnt vmcnt(11)
	ds_write_b128 v62, v[124:127] offset:64
	s_waitcnt lgkmcnt(1)
	v_mfma_f32_32x32x16_bf16 v[2:17], v[46:49], v[42:45], v[2:17]
	s_and_saveexec_b64 s[14:15], vcc
	s_cbranch_execz .LBB0_1860
	s_waitcnt vmcnt(10)
	ds_write_b128 v62, v[128:131] offset:9280
.LBB0_1860:
	s_or_b64 exec, exec, s[14:15]
	s_and_saveexec_b64 s[14:15], s[0:1]
	s_cbranch_execz .LBB0_1862
	s_waitcnt vmcnt(9)
	ds_write_b128 v63, v[132:135] offset:9280
.LBB0_1862:
	s_or_b64 exec, exec, s[14:15]
	s_waitcnt lgkmcnt(0)
	s_barrier
	global_load_dwordx4 v[124:127], v[60:61], off offset:768
	global_load_dwordx4 v[128:131], v[56:57], off offset:768
	global_load_dwordx4 v[132:135], v[58:59], off offset:768
	ds_read_b128 v[18:21], v53 offset:9280
	ds_read_b128 v[22:25], v55 offset:64
	ds_read_b128 v[26:29], v55 offset:96
	ds_read_b128 v[42:45], v53 offset:9312
	s_waitcnt lgkmcnt(2)
	v_mfma_f32_32x32x16_bf16 v[2:17], v[18:21], v[22:25], v[2:17]
	ds_read_b128 v[18:21], v53 offset:9344
	ds_read_b128 v[22:25], v55 offset:128
	s_waitcnt lgkmcnt(2)
	v_mfma_f32_32x32x16_bf16 v[2:17], v[42:45], v[26:29], v[2:17]
	ds_read_b128 v[46:49], v55 offset:160
	ds_read_b128 v[64:67], v53 offset:9376
	s_waitcnt lgkmcnt(2)
	v_mfma_f32_32x32x16_bf16 v[2:17], v[18:21], v[22:25], v[2:17]
	s_waitcnt vmcnt(11)
	ds_write_b128 v62, v[136:139] offset:27712
	s_waitcnt lgkmcnt(1)
	v_mfma_f32_32x32x16_bf16 v[2:17], v[64:67], v[46:49], v[2:17]
	s_and_saveexec_b64 s[14:15], vcc
	s_cbranch_execz .LBB0_1864
	s_waitcnt vmcnt(10)
	ds_write_b128 v62, v[140:143] offset:36928
.LBB0_1864:
	s_or_b64 exec, exec, s[14:15]
	s_and_saveexec_b64 s[14:15], s[0:1]
	s_cbranch_execz .LBB0_1866
	s_waitcnt vmcnt(9)
	ds_write_b128 v63, v[144:147] offset:36928
.LBB0_1866:
	s_or_b64 exec, exec, s[14:15]
	s_waitcnt lgkmcnt(0)
	s_barrier
	global_load_dwordx4 v[136:139], v[60:61], off offset:896
	global_load_dwordx4 v[140:143], v[56:57], off offset:896
	global_load_dwordx4 v[144:147], v[58:59], off offset:896
	ds_read_b128 v[22:25], v53 offset:36928
	ds_read_b128 v[30:33], v55 offset:27712
	ds_read_b128 v[34:37], v55 offset:27744
	ds_read_b128 v[38:41], v53 offset:36960
	s_waitcnt lgkmcnt(2)
	v_mfma_f32_32x32x16_bf16 v[2:17], v[22:25], v[30:33], v[2:17]
	s_waitcnt lgkmcnt(0)
	v_mfma_f32_32x32x16_bf16 v[2:17], v[38:41], v[34:37], v[2:17]
	ds_read_b128 v[22:25], v53 offset:36992
	ds_read_b128 v[34:37], v55 offset:27776
	ds_read_b128 v[38:41], v55 offset:27808
	ds_read_b128 v[46:49], v53 offset:37024
	s_waitcnt lgkmcnt(2)
	v_mfma_f32_32x32x16_bf16 v[2:17], v[22:25], v[34:37], v[2:17]
	s_waitcnt vmcnt(11)
	ds_write_b128 v62, v[100:103] offset:64
	s_waitcnt lgkmcnt(1)
	v_mfma_f32_32x32x16_bf16 v[2:17], v[46:49], v[38:41], v[2:17]
	s_and_saveexec_b64 s[14:15], vcc
	s_cbranch_execz .LBB0_1868
	s_waitcnt vmcnt(10)
	ds_write_b128 v62, v[104:107] offset:9280
.LBB0_1868:
	s_or_b64 exec, exec, s[14:15]
	s_and_saveexec_b64 s[14:15], s[0:1]
	s_cbranch_execz .LBB0_1870
	s_waitcnt vmcnt(9)
	ds_write_b128 v63, v[108:111] offset:9280
.LBB0_1870:
	s_or_b64 exec, exec, s[14:15]
	s_waitcnt lgkmcnt(0)
	s_barrier
	global_load_dwordx4 v[100:103], v[60:61], off offset:1024
	global_load_dwordx4 v[104:107], v[56:57], off offset:1024
	global_load_dwordx4 v[108:111], v[58:59], off offset:1024
	ds_read_b128 v[18:21], v53 offset:9280
	ds_read_b128 v[26:29], v55 offset:64
	ds_read_b128 v[38:41], v55 offset:96
	ds_read_b128 v[42:45], v53 offset:9312
	s_waitcnt lgkmcnt(2)
	v_mfma_f32_32x32x16_bf16 v[2:17], v[18:21], v[26:29], v[2:17]
	s_waitcnt lgkmcnt(0)
	v_mfma_f32_32x32x16_bf16 v[2:17], v[42:45], v[38:41], v[2:17]
	ds_read_b128 v[18:21], v53 offset:9344
	ds_read_b128 v[38:41], v55 offset:128
	ds_read_b128 v[42:45], v55 offset:160
	ds_read_b128 v[46:49], v53 offset:9376
	s_waitcnt lgkmcnt(2)
	v_mfma_f32_32x32x16_bf16 v[2:17], v[18:21], v[38:41], v[2:17]
	s_waitcnt vmcnt(11)
	ds_write_b128 v62, v[112:115] offset:27712
	s_waitcnt lgkmcnt(1)
	v_mfma_f32_32x32x16_bf16 v[2:17], v[46:49], v[42:45], v[2:17]
	s_and_saveexec_b64 s[14:15], vcc
	s_cbranch_execz .LBB0_1872
	s_waitcnt vmcnt(10)
	ds_write_b128 v62, v[116:119] offset:36928

.LBB0_1874:
	s_or_b64 exec, exec, s[14:15]
	s_waitcnt lgkmcnt(0)
	s_barrier
	global_load_dwordx4 v[112:115], v[60:61], off offset:1152
	global_load_dwordx4 v[116:119], v[56:57], off offset:1152
	global_load_dwordx4 v[120:123], v[58:59], off offset:1152
	ds_read_b128 v[22:25], v53 offset:36928
	ds_read_b128 v[30:33], v55 offset:27712
	ds_read_b128 v[34:37], v55 offset:27744
	ds_read_b128 v[42:45], v53 offset:36960
	s_waitcnt lgkmcnt(2)
	v_mfma_f32_32x32x16_bf16 v[2:17], v[22:25], v[30:33], v[2:17]
	s_waitcnt lgkmcnt(0)
	v_mfma_f32_32x32x16_bf16 v[2:17], v[42:45], v[34:37], v[2:17]
	ds_read_b128 v[22:25], v53 offset:36992
	ds_read_b128 v[34:37], v55 offset:27776
	ds_read_b128 v[42:45], v55 offset:27808
	ds_read_b128 v[46:49], v53 offset:37024
	s_waitcnt lgkmcnt(2)
	v_mfma_f32_32x32x16_bf16 v[2:17], v[22:25], v[34:37], v[2:17]
	s_waitcnt vmcnt(11)
	ds_write_b128 v62, v[124:127] offset:64
	s_waitcnt lgkmcnt(1)
	v_mfma_f32_32x32x16_bf16 v[2:17], v[46:49], v[42:45], v[2:17]
	s_and_saveexec_b64 s[14:15], vcc
	s_cbranch_execz .LBB0_1876
	s_waitcnt vmcnt(10)
	ds_write_b128 v62, v[128:131] offset:9280

.LBB0_1878:
	s_or_b64 exec, exec, s[14:15]
	s_waitcnt lgkmcnt(0)
	s_barrier
	global_load_dwordx4 v[124:127], v[60:61], off offset:1280
	global_load_dwordx4 v[128:131], v[56:57], off offset:1280
	global_load_dwordx4 v[132:135], v[58:59], off offset:1280
	ds_read_b128 v[18:21], v53 offset:9280
	ds_read_b128 v[26:29], v55 offset:64
	ds_read_b128 v[38:41], v55 offset:96
	ds_read_b128 v[42:45], v53 offset:9312
	s_waitcnt lgkmcnt(2)
	v_mfma_f32_32x32x16_bf16 v[2:17], v[18:21], v[26:29], v[2:17]
	s_waitcnt lgkmcnt(0)
	v_mfma_f32_32x32x16_bf16 v[2:17], v[42:45], v[38:41], v[2:17]
	ds_read_b128 v[18:21], v53 offset:9344
	ds_read_b128 v[38:41], v55 offset:128
	ds_read_b128 v[42:45], v55 offset:160
	ds_read_b128 v[46:49], v53 offset:9376
	s_waitcnt lgkmcnt(2)
	v_mfma_f32_32x32x16_bf16 v[2:17], v[18:21], v[38:41], v[2:17]
	s_waitcnt vmcnt(11)
	ds_write_b128 v62, v[136:139] offset:27712
	s_waitcnt lgkmcnt(1)
	v_mfma_f32_32x32x16_bf16 v[2:17], v[46:49], v[42:45], v[2:17]
	s_and_saveexec_b64 s[14:15], vcc
	s_cbranch_execz .LBB0_1880
	s_waitcnt vmcnt(10)
	ds_write_b128 v62, v[140:143] offset:36928

.LBB0_1882:
	s_or_b64 exec, exec, s[14:15]
	s_waitcnt lgkmcnt(0)
	s_barrier
	global_load_dwordx4 v[136:139], v[60:61], off offset:1408
	global_load_dwordx4 v[140:143], v[56:57], off offset:1408
	global_load_dwordx4 v[144:147], v[58:59], off offset:1408
	ds_read_b128 v[22:25], v53 offset:36928
	ds_read_b128 v[30:33], v55 offset:27712
	ds_read_b128 v[34:37], v55 offset:27744
	ds_read_b128 v[42:45], v53 offset:36960
	s_waitcnt lgkmcnt(2)
	v_mfma_f32_32x32x16_bf16 v[2:17], v[22:25], v[30:33], v[2:17]
	s_waitcnt lgkmcnt(0)
	v_mfma_f32_32x32x16_bf16 v[2:17], v[42:45], v[34:37], v[2:17]
	ds_read_b128 v[22:25], v53 offset:36992
	ds_read_b128 v[34:37], v55 offset:27776
	ds_read_b128 v[42:45], v55 offset:27808
	ds_read_b128 v[46:49], v53 offset:37024
	s_waitcnt lgkmcnt(2)
	v_mfma_f32_32x32x16_bf16 v[2:17], v[22:25], v[34:37], v[2:17]
	s_waitcnt vmcnt(11)
	ds_write_b128 v62, v[100:103] offset:64
	s_waitcnt lgkmcnt(1)
	v_mfma_f32_32x32x16_bf16 v[2:17], v[46:49], v[42:45], v[2:17]
	s_and_saveexec_b64 s[14:15], vcc
	s_cbranch_execz .LBB0_1884
	s_waitcnt vmcnt(10)
	ds_write_b128 v62, v[104:107] offset:9280

.LBB0_1886:
	s_or_b64 exec, exec, s[14:15]
	s_waitcnt lgkmcnt(0)
	s_barrier
	global_load_dwordx4 v[100:103], v[60:61], off offset:1536
	global_load_dwordx4 v[104:107], v[56:57], off offset:1536
	global_load_dwordx4 v[108:111], v[58:59], off offset:1536
	ds_read_b128 v[18:21], v53 offset:9280
	ds_read_b128 v[26:29], v55 offset:64
	ds_read_b128 v[38:41], v55 offset:96
	ds_read_b128 v[42:45], v53 offset:9312
	s_waitcnt lgkmcnt(2)
	v_mfma_f32_32x32x16_bf16 v[2:17], v[18:21], v[26:29], v[2:17]
	s_waitcnt lgkmcnt(0)
	v_mfma_f32_32x32x16_bf16 v[2:17], v[42:45], v[38:41], v[2:17]
	ds_read_b128 v[18:21], v53 offset:9344
	ds_read_b128 v[38:41], v55 offset:128
	ds_read_b128 v[42:45], v55 offset:160
	ds_read_b128 v[46:49], v53 offset:9376
	s_waitcnt lgkmcnt(2)
	v_mfma_f32_32x32x16_bf16 v[2:17], v[18:21], v[38:41], v[2:17]
	s_waitcnt vmcnt(11)
	ds_write_b128 v62, v[112:115] offset:27712
	s_waitcnt lgkmcnt(1)
	v_mfma_f32_32x32x16_bf16 v[2:17], v[46:49], v[42:45], v[2:17]
	s_and_saveexec_b64 s[14:15], vcc
	s_cbranch_execz .LBB0_1888
	s_waitcnt vmcnt(10)
	ds_write_b128 v62, v[116:119] offset:36928

.LBB0_1890:
	s_or_b64 exec, exec, s[14:15]
	s_waitcnt lgkmcnt(0)
	s_barrier
	global_load_dwordx4 v[112:115], v[60:61], off offset:1664
	global_load_dwordx4 v[116:119], v[56:57], off offset:1664
	global_load_dwordx4 v[120:123], v[58:59], off offset:1664
	ds_read_b128 v[22:25], v53 offset:36928
	ds_read_b128 v[30:33], v55 offset:27712
	ds_read_b128 v[34:37], v55 offset:27744
	ds_read_b128 v[42:45], v53 offset:36960
	s_waitcnt lgkmcnt(2)
	v_mfma_f32_32x32x16_bf16 v[2:17], v[22:25], v[30:33], v[2:17]
	s_waitcnt lgkmcnt(0)
	v_mfma_f32_32x32x16_bf16 v[2:17], v[42:45], v[34:37], v[2:17]
	ds_read_b128 v[22:25], v53 offset:36992
	ds_read_b128 v[34:37], v55 offset:27776
	ds_read_b128 v[42:45], v55 offset:27808
	ds_read_b128 v[46:49], v53 offset:37024
	s_waitcnt lgkmcnt(2)
	v_mfma_f32_32x32x16_bf16 v[2:17], v[22:25], v[34:37], v[2:17]
	s_waitcnt vmcnt(11)
	ds_write_b128 v62, v[124:127] offset:64
	s_waitcnt lgkmcnt(1)
	v_mfma_f32_32x32x16_bf16 v[2:17], v[46:49], v[42:45], v[2:17]
	s_and_saveexec_b64 s[14:15], vcc
	s_cbranch_execz .LBB0_1892
	s_waitcnt vmcnt(10)
	ds_write_b128 v62, v[128:131] offset:9280

.LBB0_1894:
	s_or_b64 exec, exec, s[14:15]
	s_waitcnt lgkmcnt(0)
	s_barrier
	global_load_dwordx4 v[124:127], v[60:61], off offset:1792
	global_load_dwordx4 v[128:131], v[56:57], off offset:1792
	global_load_dwordx4 v[132:135], v[58:59], off offset:1792
	ds_read_b128 v[18:21], v53 offset:9280
	ds_read_b128 v[26:29], v55 offset:64
	ds_read_b128 v[38:41], v55 offset:96
	ds_read_b128 v[42:45], v53 offset:9312
	s_waitcnt lgkmcnt(2)
	v_mfma_f32_32x32x16_bf16 v[2:17], v[18:21], v[26:29], v[2:17]
	s_waitcnt lgkmcnt(0)
	v_mfma_f32_32x32x16_bf16 v[2:17], v[42:45], v[38:41], v[2:17]
	ds_read_b128 v[18:21], v53 offset:9344
	ds_read_b128 v[38:41], v55 offset:128
	ds_read_b128 v[42:45], v55 offset:160
	ds_read_b128 v[46:49], v53 offset:9376
	s_waitcnt lgkmcnt(2)
	v_mfma_f32_32x32x16_bf16 v[2:17], v[18:21], v[38:41], v[2:17]
	s_waitcnt vmcnt(11)
	ds_write_b128 v62, v[136:139] offset:27712
	s_waitcnt lgkmcnt(1)
	v_mfma_f32_32x32x16_bf16 v[2:17], v[46:49], v[42:45], v[2:17]
	s_and_saveexec_b64 s[14:15], vcc
	s_cbranch_execz .LBB0_1896
	s_waitcnt vmcnt(10)
	ds_write_b128 v62, v[140:143] offset:36928

.LBB0_1898:
	s_or_b64 exec, exec, s[14:15]
	s_waitcnt lgkmcnt(0)
	s_barrier
	global_load_dwordx4 v[136:139], v[60:61], off offset:1920
	global_load_dwordx4 v[140:143], v[56:57], off offset:1920
	global_load_dwordx4 v[144:147], v[58:59], off offset:1920
	ds_read_b128 v[22:25], v53 offset:36928
	ds_read_b128 v[30:33], v55 offset:27712
	ds_read_b128 v[34:37], v55 offset:27744
	ds_read_b128 v[42:45], v53 offset:36960
	s_waitcnt lgkmcnt(2)
	v_mfma_f32_32x32x16_bf16 v[2:17], v[22:25], v[30:33], v[2:17]
	ds_read_b128 v[22:25], v53 offset:36992
	ds_read_b128 v[30:33], v55 offset:27776
	s_waitcnt lgkmcnt(2)
	v_mfma_f32_32x32x16_bf16 v[2:17], v[42:45], v[34:37], v[2:17]
	ds_read_b128 v[34:37], v55 offset:27808
	ds_read_b128 v[64:67], v53 offset:37024
	s_waitcnt lgkmcnt(2)
	v_mfma_f32_32x32x16_bf16 v[2:17], v[22:25], v[30:33], v[2:17]
	s_waitcnt vmcnt(11)
	ds_write_b128 v62, v[100:103] offset:64
	s_waitcnt lgkmcnt(1)
	v_mfma_f32_32x32x16_bf16 v[2:17], v[64:67], v[34:37], v[2:17]
	s_and_saveexec_b64 s[14:15], vcc
	s_cbranch_execz .LBB0_1900
	s_waitcnt vmcnt(10)
	ds_write_b128 v62, v[104:107] offset:9280

.LBB0_1902:
	s_or_b64 exec, exec, s[14:15]
	s_waitcnt lgkmcnt(0)
	s_barrier
	ds_read_b128 v[18:21], v53 offset:9280
	ds_read_b128 v[26:29], v55 offset:64
	ds_read_b128 v[30:33], v55 offset:96
	ds_read_b128 v[34:37], v53 offset:9312
	s_waitcnt lgkmcnt(2)
	v_mfma_f32_32x32x16_bf16 v[2:17], v[18:21], v[26:29], v[2:17]
	ds_read_b128 v[18:21], v53 offset:9344
	ds_read_b128 v[26:29], v55 offset:128
	s_waitcnt lgkmcnt(2)
	v_mfma_f32_32x32x16_bf16 v[2:17], v[34:37], v[30:33], v[2:17]
	ds_read_b128 v[64:67], v55 offset:160
	ds_read_b128 v[68:71], v53 offset:9376
	s_waitcnt vmcnt(8)
	ds_write_b128 v62, v[112:115] offset:27712
	s_waitcnt lgkmcnt(3)
	v_mfma_f32_32x32x16_bf16 v[2:17], v[18:21], v[26:29], v[2:17]
	s_waitcnt lgkmcnt(1)
	v_mfma_f32_32x32x16_bf16 v[2:17], v[68:71], v[64:67], v[2:17]
	s_and_saveexec_b64 s[14:15], vcc
	s_cbranch_execz .LBB0_1904
	s_waitcnt vmcnt(7)
	ds_write_b128 v62, v[116:119] offset:36928
.LBB0_1904:
	s_or_b64 exec, exec, s[14:15]
	s_and_saveexec_b64 s[14:15], s[0:1]
	s_cbranch_execz .LBB0_1906
	s_waitcnt vmcnt(6)
	ds_write_b128 v63, v[120:123] offset:36928
.LBB0_1906:
	s_or_b64 exec, exec, s[14:15]
	s_waitcnt lgkmcnt(0)
	s_barrier
	ds_read_b128 v[42:45], v53 offset:36928
	ds_read_b128 v[46:49], v55 offset:27712
	s_waitcnt lgkmcnt(0)
	v_mfma_f32_32x32x16_bf16 v[2:17], v[42:45], v[46:49], v[2:17]
	ds_read_b128 v[42:45], v53 offset:36960
	ds_read_b128 v[46:49], v55 offset:27744
	s_waitcnt lgkmcnt(0)
	v_mfma_f32_32x32x16_bf16 v[2:17], v[42:45], v[46:49], v[2:17]
	ds_read_b128 v[42:45], v53 offset:36992
	ds_read_b128 v[46:49], v55 offset:27776
	s_waitcnt lgkmcnt(0)
	v_mfma_f32_32x32x16_bf16 v[2:17], v[42:45], v[46:49], v[2:17]
	ds_read_b128 v[42:45], v53 offset:37024
	ds_read_b128 v[46:49], v55 offset:27808
	s_waitcnt vmcnt(5)
	ds_write_b128 v62, v[124:127] offset:64
	s_waitcnt lgkmcnt(1)
	v_mfma_f32_32x32x16_bf16 v[2:17], v[42:45], v[46:49], v[2:17]
	s_and_saveexec_b64 s[14:15], vcc
	s_cbranch_execz .LBB0_1908
	s_waitcnt vmcnt(4)
	ds_write_b128 v62, v[128:131] offset:9280
.LBB0_1908:
	s_or_b64 exec, exec, s[14:15]
	s_and_saveexec_b64 s[14:15], s[0:1]
	s_cbranch_execz .LBB0_1910
	s_waitcnt vmcnt(3)
	ds_write_b128 v63, v[132:135] offset:9280
.LBB0_1910:
	s_or_b64 exec, exec, s[14:15]
	s_waitcnt lgkmcnt(0)
	s_barrier
	ds_read_b128 v[30:33], v53 offset:9280
	ds_read_b128 v[34:37], v55 offset:64
	s_waitcnt lgkmcnt(0)
	v_mfma_f32_32x32x16_bf16 v[2:17], v[30:33], v[34:37], v[2:17]
	ds_read_b128 v[30:33], v53 offset:9312
	ds_read_b128 v[34:37], v55 offset:96
	s_waitcnt lgkmcnt(0)
	v_mfma_f32_32x32x16_bf16 v[2:17], v[30:33], v[34:37], v[2:17]
	ds_read_b128 v[30:33], v53 offset:9344
	ds_read_b128 v[34:37], v55 offset:128
	s_waitcnt lgkmcnt(0)
	v_mfma_f32_32x32x16_bf16 v[2:17], v[30:33], v[34:37], v[2:17]
	ds_read_b128 v[30:33], v53 offset:9376
	ds_read_b128 v[34:37], v55 offset:160
	s_waitcnt vmcnt(2)
	ds_write_b128 v62, v[136:139] offset:27712
	s_waitcnt lgkmcnt(1)
	v_mfma_f32_32x32x16_bf16 v[2:17], v[30:33], v[34:37], v[2:17]
	s_and_saveexec_b64 s[14:15], vcc
	s_cbranch_execz .LBB0_1912
	s_waitcnt vmcnt(1)
	ds_write_b128 v62, v[140:143] offset:36928
.LBB0_1912:
	s_or_b64 exec, exec, s[14:15]
	s_and_saveexec_b64 s[14:15], s[0:1]
	s_cbranch_execz .LBB0_1849
	s_waitcnt vmcnt(0)
	ds_write_b128 v63, v[144:147] offset:36928
	s_branch .LBB0_1849
